# trimmed MLA loop instruction stream (peeled first/drain intervals, merged LDS waits), background MoE weight conversion after the per-interval vmcnt(0) with scalar-stepped saddr loads, static s_setprio
# speedup vs baseline: 1.0194x; 1.0194x over previous
.LBB0_1007:
	s_cmp_lt_i32 s80, 1
	s_cbranch_scc1 .LBB0_1153
	v_bfe_u32 v4, v0, 5, 1
	v_lshrrev_b32_e32 v3, 1, v0
	v_lshlrev_b32_e32 v1, 7, v156
	v_bfe_u32 v5, v0, 1, 3
	v_bitop3_b32 v3, v4, v3, 7 bitop3:0x78
	v_lshl_or_b32 v200, v3, 4, v1
	v_bitop3_b32 v3, v4, v5, 2 bitop3:0x36
	v_lshl_or_b32 v201, v3, 4, v1
	v_bitop3_b32 v3, v4, v5, 4 bitop3:0x36
	v_lshlrev_b32_e32 v202, 4, v3
	v_bitop3_b32 v3, v4, v5, 6 bitop3:0x36
	v_lshlrev_b32_e32 v203, 4, v3
	v_add_u32_e32 v202, v202, v1
	v_add_u32_e32 v203, v203, v1
	s_mov_b32 s83, 0
	v_lshlrev_b32_e32 v3, 4, v0
	v_and_b32_e32 v5, 0x3c0, v3
	v_xor_b32_e32 v3, v3, v0
	v_and_or_b32 v206, v3, 48, v5
	v_lshrrev_b32_e32 v3, 2, v0
	v_lshlrev_b32_e32 v7, 1, v4
	v_bfe_u32 v5, v0, 2, 2
	v_lshl_add_u32 v6, v156, 6, 0
	v_bitop3_b32 v3, v7, v3, 3 bitop3:0x78
	v_writelane_b32 v238, s96, 41
	v_and_b32_e32 v2, 63, v0
	v_lshl_add_u32 v207, v3, 4, v6
	v_bitop3_b32 v3, v7, v5, 1 bitop3:0x36
	v_writelane_b32 v238, s97, 42
	v_lshlrev_b32_e32 v204, 2, v4
	v_lshl_add_u32 v208, v3, 4, v6
	v_mov_b32_e32 v3, 0
	v_cmp_gt_u32_e64 s[0:1], 32, v2
	v_and_b32_e32 v2, 3, v0
	v_lshlrev_b32_e32 v164, 13, v4
	v_writelane_b32 v238, s92, 37
	v_bfe_u32 v205, v0, 3, 3
	s_mov_b32 s71, 0
	v_mov_b32_e32 v157, v3
	v_lshlrev_b32_e32 v158, 11, v156
	v_mov_b32_e32 v159, v3
	v_lshlrev_b32_e32 v160, 4, v4
	v_mov_b32_e32 v161, v3
	v_lshlrev_b32_e32 v162, 10, v156
	v_mov_b32_e32 v163, v3
	v_cmp_eq_u32_e64 s[2:3], 0, v2
	v_mov_b32_e32 v165, v3
	v_or_b32_e32 v166, 0x1000, v164
	v_mov_b32_e32 v167, v3
	v_or_b32_e32 v168, 0x1800, v164
	v_mov_b32_e32 v169, v3
	v_or_b32_e32 v170, 0x4000, v164
	v_mov_b32_e32 v171, v3
	v_or_b32_e32 v172, 0x4800, v164
	v_mov_b32_e32 v173, v3
	v_or_b32_e32 v174, 0x5000, v164
	v_mov_b32_e32 v175, v3
	v_or_b32_e32 v176, 0x5800, v164
	v_mov_b32_e32 v177, v3
	v_or_b32_e32 v178, 0x8000, v164
	v_mov_b32_e32 v179, v3
	v_or_b32_e32 v180, 0x8800, v164
	v_mov_b32_e32 v181, v3
	v_or_b32_e32 v182, 0x9000, v164
	v_mov_b32_e32 v183, v3
	v_or_b32_e32 v184, 0x9800, v164
	v_mov_b32_e32 v185, v3
	v_or_b32_e32 v186, 0xc000, v164
	v_mov_b32_e32 v187, v3
	v_or_b32_e32 v188, 0xc800, v164
	v_mov_b32_e32 v189, v3
	v_or_b32_e32 v190, 0xd000, v164
	v_mov_b32_e32 v191, v3
	v_or_b32_e32 v192, 0xd800, v164
	v_mov_b32_e32 v193, v3
	v_sub_u32_e32 v209, v156, v204
	s_add_i32 s81, 0, 0x8000
	s_mov_b64 s[88:89], 0x20000
	s_mov_b64 s[68:69], 0x2000
	s_mov_b32 s96, 0x3ad53b94
	v_mov_b32_e32 v210, 0x40a00000
	s_mov_b32 s33, 0xc3e00000
	v_mov_b32_e32 v211, 0xff800000
	v_mov_b32_e32 v212, 0x43e00000
	s_mov_b32 s94, 0
	v_writelane_b32 v238, s93, 38
	s_branch .LBB0_1010

.LBB0_1010:
	s_lshr_b32 s4, s94, 1
	s_mul_i32 s4, s4, s82
	v_readlane_b32 s5, v236, 34
	s_add_i32 s5, s4, s5
	s_and_b32 s4, s5, 7
	s_ashr_i32 s6, s5, 5
	s_lshl_b32 s5, s5, 5
	s_and_b32 s6, s6, -8
	s_and_b32 s5, s5, 0x1f00
	s_or_b32 s4, s6, s4
	s_and_b32 s6, s94, 1
	s_xor_b32 s7, s5, 0x3f00
	v_readlane_b32 s12, v237, 61
	s_cmp_eq_u32 s6, 0
	v_readlane_b32 s13, v237, 62
	v_readlane_b32 s14, v237, 63
	v_readlane_b32 s15, v238, 0
	v_readlane_b32 s16, v238, 1
	v_readlane_b32 s17, v238, 2
	v_readlane_b32 s18, v238, 3
	v_readlane_b32 s19, v238, 4
	v_readlane_b32 s20, v238, 5
	v_readlane_b32 s21, v238, 6
	v_readlane_b32 s22, v238, 7
	v_readlane_b32 s23, v238, 8
	s_cselect_b32 s8, s5, s7
	v_readlane_b32 s24, v238, 9
	v_readlane_b32 s25, v238, 10
	v_readlane_b32 s26, v238, 11
	v_readlane_b32 s27, v238, 12
	s_mov_b64 s[12:13], s[16:17]
	s_lshl_b32 s97, s8, 11
	s_mov_b64 s[14:15], s[18:19]
	s_mov_b64 s[16:17], s[20:21]
	s_mov_b64 s[18:19], s[22:23]
	s_add_u32 s5, s18, s97
	s_addc_u32 s6, s19, 0
	s_lshl_b32 s66, s4, 7
	s_ashr_i32 s67, s66, 31
	s_add_u32 s9, s5, s66
	s_mov_b64 s[20:21], s[24:25]
	s_addc_u32 s10, s6, s67
	s_lshl_b32 s5, s8, 10
	s_add_u32 s5, s20, s5
	s_addc_u32 s6, s21, 0
	s_lshl_b32 s7, s4, 6
	s_ashr_i32 s11, s7, 31
	s_add_u32 s12, s5, s7
	s_mov_b64 s[22:23], s[26:27]
	s_addc_u32 s11, s6, s11
	s_add_u32 s6, s22, s66
	s_addc_u32 s7, s23, s67
	s_ashr_i32 s5, s4, 31
	s_lshl_b64 s[4:5], s[4:5], 21
	s_add_u32 s4, s84, s4
	v_readfirstlane_b32 s13, v0
	s_addc_u32 s5, s85, s5
	s_lshr_b32 s14, s13, 6
	s_lshl_b32 s70, s14, 5
	s_lshr_b32 s72, s8, 6
	s_add_i32 s95, s70, s8
	s_and_b32 s8, s13, 0x3fffffc0
	s_lshl_b32 s8, s8, 2
	s_add_i32 s8, s8, 0
	s_add_i32 s13, s8, 0x14000
	s_add_i32 s72, s72, 4
	s_lshl_b32 s74, s14, 10
	s_cmp_lg_u32 0, -1
	s_cselect_b32 s8, 0, 0
	s_add_i32 s73, s74, s8
	s_cmp_lg_u32 s81, -1
	s_cselect_b32 s8, s81, 0
	v_or_b32_e32 v6, s74, v206
	s_add_i32 s74, s74, s8
	s_add_i32 s75, s74, 0x8000
	s_lshl_b64 s[92:93], s[70:71], 11
	s_add_u32 s8, s9, s92
	s_addc_u32 s9, s10, s93
	v_lshl_add_u64 v[8:9], s[8:9], 0, v[158:159]
	s_lshl_b64 s[8:9], s[70:71], 10
	s_add_u32 s8, s12, s8
	s_addc_u32 s9, s11, s9
	v_lshl_add_u64 v[8:9], v[8:9], 0, v[160:161]
	v_lshl_add_u64 v[10:11], s[8:9], 0, v[162:163]
	v_lshl_add_u64 v[10:11], v[10:11], 0, v[160:161]
	global_load_dwordx4 v[100:103], v[8:9], off
	global_load_dwordx4 v[104:107], v[8:9], off offset:32
	global_load_dwordx4 v[108:111], v[8:9], off offset:64
	global_load_dwordx4 v[112:115], v[8:9], off offset:96
	global_load_dwordx4 v[116:119], v[10:11], off
	global_load_dwordx4 v[120:123], v[10:11], off offset:32
	v_lshl_or_b32 v4, s14, 3, v205
	v_lshrrev_b32_e32 v2, 1, v4
	v_xor_b32_e32 v2, v2, v0
	v_lshlrev_b32_e32 v2, 4, v2
	v_and_b32_e32 v5, 0x70, v2
	v_lshl_or_b32 v2, v4, 11, v5
	v_lshl_or_b32 v4, v4, 7, v5
	v_lshl_add_u64 v[8:9], s[6:7], 0, v[2:3]
	s_mov_b32 s6, m0
	s_mov_b32 m0, s74
	s_nop 0
	global_load_lds_dwordx4 v[8:9], off
	s_mov_b32 m0, s6
	v_mov_b32_e32 v5, v3
	v_lshl_add_u64 v[4:5], s[16:17], 0, v[4:5]
	s_mov_b32 s6, m0
	s_mov_b32 m0, s75
	s_nop 0
	global_load_lds_dwordx4 v[4:5], off
	s_mov_b32 m0, s6
	v_mov_b32_e32 v7, v3
	v_lshl_add_u64 v[6:7], s[4:5], 0, v[6:7]
	s_mov_b32 s4, m0
	s_mov_b32 m0, s73
	s_nop 0
	global_load_lds_dwordx4 v[6:7], off
	s_mov_b32 m0, s4
	v_mov_b32_e32 v16, v3
	v_mov_b32_e32 v17, v3
	s_waitcnt vmcnt(0) lgkmcnt(0)
	s_barrier
	v_lshl_add_u64 v[194:195], v[8:9], 0, s[88:89]
	v_lshl_add_u64 v[196:197], v[4:5], 0, s[68:69]
	v_lshl_add_u64 v[198:199], v[6:7], 0, s[68:69]
	v_mov_b32_e32 v2, v3
	v_mov_b32_e32 v4, v3
	v_mov_b32_e32 v5, v3
	v_mov_b32_e32 v6, v3
	v_mov_b32_e32 v7, v3
	v_mov_b32_e32 v8, v3
	v_mov_b32_e32 v9, v3
	v_mov_b32_e32 v10, v3
	v_mov_b32_e32 v11, v3
	v_mov_b32_e32 v12, v3
	v_mov_b32_e32 v13, v3
	v_mov_b32_e32 v14, v3
	v_mov_b32_e32 v15, v3
	v_mov_b64_e32 v[66:67], v[16:17]
	v_mov_b64_e32 v[50:51], v[16:17]
	v_mov_b64_e32 v[34:35], v[16:17]
	v_mov_b64_e32 v[64:65], v[14:15]
	v_mov_b64_e32 v[62:63], v[12:13]
	v_mov_b64_e32 v[60:61], v[10:11]
	v_mov_b64_e32 v[58:59], v[8:9]
	v_mov_b64_e32 v[56:57], v[6:7]
	v_mov_b64_e32 v[54:55], v[4:5]
	v_mov_b64_e32 v[52:53], v[2:3]
	v_mov_b64_e32 v[48:49], v[14:15]
	v_mov_b64_e32 v[46:47], v[12:13]
	v_mov_b64_e32 v[44:45], v[10:11]
	v_mov_b64_e32 v[42:43], v[8:9]
	v_mov_b64_e32 v[40:41], v[6:7]
	v_mov_b64_e32 v[38:39], v[4:5]
	v_mov_b64_e32 v[36:37], v[2:3]
	v_mov_b64_e32 v[32:33], v[14:15]
	v_mov_b64_e32 v[30:31], v[12:13]
	v_mov_b64_e32 v[28:29], v[10:11]
	v_mov_b64_e32 v[26:27], v[8:9]
	v_mov_b64_e32 v[24:25], v[6:7]
	v_mov_b64_e32 v[22:23], v[4:5]
	v_mov_b64_e32 v[20:21], v[2:3]
	v_mov_b64_e32 v[18:19], v[16:17]
	s_or_b32 s70, s95, 31
	v_lshl_add_u32 v214, v156, 2, s13
	v_lshl_add_u32 v213, v204, 2, s13
	v_add_u32_e32 v215, s95, v209
	v_mov_b32_e32 v216, 0xf149f2ca
	s_mov_b32 s76, 63
	v_mov_b64_e32 v[16:17], v[14:15]
	v_mov_b64_e32 v[14:15], v[12:13]
	v_mov_b64_e32 v[12:13], v[10:11]
	v_mov_b64_e32 v[10:11], v[8:9]
	v_mov_b64_e32 v[8:9], v[6:7]
	v_mov_b64_e32 v[6:7], v[4:5]
	v_mov_b64_e32 v[4:5], v[2:3]
	s_mov_b32 s77, 0
	v_mov_b32_e32 v2, 0
	s_mov_b32 s40, m0
	s_lshr_b32 s4, s70, 6
	s_add_i32 s4, s4, 1
	s_min_u32 s42, s4, s72
	s_lshr_b32 s43, s95, 6
	v_add_u32_e32 v242, 0x10000, v200
	v_add_u32_e32 v243, 0x10000, v201
	v_readlane_b32 s37, v236, 34
	v_readfirstlane_b32 s4, v0
	s_nop 3
	s_lshr_b32 s36, s4, 6
	s_lshr_b32 s5, s37, 6
	s_lshl_b32 s5, s5, 7
	s_lshl_b32 s6, s36, 4
	s_add_i32 s5, s5, s6
	s_and_b32 s7, s37, 63
	s_lshl_b32 s8, s5, 14
	s_lshl_b32 s9, s7, 8
	s_add_i32 s8, s8, s9
	v_readlane_b32 s52, v237, 29
	v_readlane_b32 s53, v237, 30
	s_add_u32 s52, s52, s8
	s_addc_u32 s53, s53, 0
	s_bfe_u32 s8, s7, 0x40001
	s_lshl_b32 s8, s8, 8
	s_and_b32 s9, s7, 1
	s_lshl_b32 s9, s9, 6
	s_add_i32 s8, s8, s9
	s_lshr_b32 s9, s7, 5
	s_lshl_b32 s9, s9, 7
	s_add_i32 s8, s8, s9
	s_lshl_b32 s8, s8, 11
	s_add_i32 s8, s8, s5
	v_readlane_b32 s54, v237, 51
	v_readlane_b32 s55, v237, 52
	s_add_u32 s54, s54, s8
	s_addc_u32 s55, s55, 0
	s_lshr_b32 s5, s37, 5
	s_lshl_b32 s5, s5, 7
	s_add_i32 s5, s5, s6
	s_and_b32 s7, s37, 31
	s_lshl_b32 s8, s5, 13
	s_lshl_b32 s9, s7, 8
	s_add_i32 s8, s8, s9
	v_readlane_b32 s58, v237, 33
	v_readlane_b32 s59, v237, 34
	s_add_u32 s58, s58, s8
	s_addc_u32 s59, s59, 0
	s_lshl_b32 s8, s7, 17
	s_add_i32 s8, s8, s5
	v_readlane_b32 s60, v237, 53
	v_readlane_b32 s61, v237, 54
	s_add_u32 s60, s60, s8
	s_addc_u32 s61, s61, 0
	s_mov_b32 s50, 0x44000000
	s_mov_b32 s51, 0x44000000
	s_mov_b32 s47, 0
	s_mov_b32 s48, 0
	v_and_b32_e32 v241, 63, v0
	v_lshlrev_b32_e32 v240, 11, v241
	v_lshlrev_b32_e32 v241, 2, v241
	s_cmp_ge_u32 s36, 4
	s_cbranch_scc1 .Lm_Lstart
.Lm_Estart:
	s_add_i32 s4, s77, 1
	s_cmp_ge_u32 s4, s72
	s_cbranch_scc1 .Lm_nd1
	s_add_i32 m0, s74, 0x4000
	s_add_i32 s8, s75, 0x2000
	global_load_lds_dwordx4 v[194:195], off
	s_mov_b32 m0, s8
	s_add_i32 s8, s73, 0x4000
	global_load_lds_dwordx4 v[196:197], off
	s_mov_b32 m0, s8
	s_nop 0
	global_load_lds_dwordx4 v[198:199], off
.Lm_nd1:
	ds_read_b128 v[166:169], v200 offset:32768
	ds_read_b128 v[174:177], v200 offset:36864
	ds_read_b128 v[170:173], v201 offset:32768
	ds_read_b128 v[178:181], v201 offset:36864
	ds_read_b128 v[182:185], v202 offset:32768
	ds_read_b128 v[218:221], v202 offset:36864
	ds_read_b128 v[186:189], v203 offset:32768
	ds_read_b128 v[222:225], v203 offset:36864
	s_waitcnt lgkmcnt(4)
	v_mfma_f32_32x32x64_f8f6f4 v[68:83], v[166:173], v[100:107], 0
	v_mfma_f32_32x32x64_f8f6f4 v[84:99], v[174:181], v[100:107], 0
	ds_read_b128 v[166:169], v242 offset:0
	ds_read_b128 v[174:177], v242 offset:4096
	ds_read_b128 v[170:173], v243 offset:0
	ds_read_b128 v[178:181], v243 offset:4096
	s_waitcnt lgkmcnt(4)
	v_mfma_f32_32x32x64_f8f6f4 v[68:83], v[182:189], v[108:115], v[68:83]
	v_mfma_f32_32x32x64_f8f6f4 v[84:99], v[218:225], v[108:115], v[84:99]
	s_waitcnt lgkmcnt(0)
	v_mfma_f32_32x32x64_f8f6f4 v[68:83], v[166:173], v[116:123], v[68:83]
	v_mfma_f32_32x32x64_f8f6f4 v[84:99], v[174:181], v[116:123], v[84:99]
	s_waitcnt vmcnt(0) lgkmcnt(0)
	s_cmp_eq_u32 s48, 0
	s_cbranch_scc1 .Lm_bf3
	v_pk_mul_f32 v[226:227], v[226:227], s[50:51]
	v_pk_mul_f32 v[228:229], v[228:229], s[50:51]
	v_pk_mul_f32 v[230:231], v[230:231], s[50:51]
	v_pk_mul_f32 v[232:233], v[232:233], s[50:51]
	v_med3_f32 v226, v226, s33, v212
	v_med3_f32 v227, v227, s33, v212
	v_med3_f32 v228, v228, s33, v212
	v_med3_f32 v229, v229, s33, v212
	v_med3_f32 v230, v230, s33, v212
	v_med3_f32 v231, v231, s33, v212
	v_med3_f32 v232, v232, s33, v212
	v_med3_f32 v233, v233, s33, v212
	v_cvt_pk_fp8_f32 v246, v226, v227
	v_cvt_pk_fp8_f32 v247, v230, v231
	v_cvt_pk_fp8_f32 v246, v228, v229 op_sel:[0,0,1]
	v_cvt_pk_fp8_f32 v247, v232, v233 op_sel:[0,0,1]
	global_store_dwordx4 v240, v[244:247], s[44:45]
	s_mov_b32 s48, 0
.Lm_bf3:
	s_cmp_ge_u32 s83, 192
	s_cbranch_scc1 .Lm_bs2
	s_cmp_ge_u32 s83, 128
	s_cbranch_scc1 .Lm_dn4
	s_lshl_b32 s4, s83, 23
	s_add_u32 s14, s52, s4
	s_addc_u32 s15, s53, 0
	s_lshr_b32 s4, s83, 2
	s_lshl_b32 s4, s4, 23
	s_and_b32 s5, s83, 3
	s_lshl_b32 s5, s5, 9
	s_add_i32 s4, s4, s5
	s_add_u32 s44, s54, s4
	s_addc_u32 s45, s55, 0
	s_mov_b32 s46, 0x4000
	s_branch .Lm_dd4
.Lm_dn4:
	s_sub_i32 s6, s83, 128
	s_lshl_b32 s4, s6, 23
	s_add_u32 s14, s58, s4
	s_addc_u32 s15, s59, 0
	s_lshr_b32 s4, s6, 1
	s_lshl_b32 s4, s4, 22
	s_and_b32 s5, s6, 1
	s_lshl_b32 s5, s5, 10
	s_add_i32 s4, s4, s5
	s_add_u32 s44, s60, s4
	s_addc_u32 s45, s61, 0
	s_mov_b32 s46, 0x2000
.Lm_dd4:
	global_load_dword v226, v241, s[14:15]
	s_add_u32 s14, s14, s46
	s_addc_u32 s15, s15, 0
	global_load_dword v227, v241, s[14:15]
	s_add_u32 s14, s14, s46
	s_addc_u32 s15, s15, 0
	global_load_dword v228, v241, s[14:15]
	s_add_u32 s14, s14, s46
	s_addc_u32 s15, s15, 0
	global_load_dword v229, v241, s[14:15]
	s_add_u32 s14, s14, s46
	s_addc_u32 s15, s15, 0
	global_load_dword v230, v241, s[14:15]
	s_add_u32 s14, s14, s46
	s_addc_u32 s15, s15, 0
	global_load_dword v231, v241, s[14:15]
	s_add_u32 s14, s14, s46
	s_addc_u32 s15, s15, 0
	global_load_dword v232, v241, s[14:15]
	s_add_u32 s14, s14, s46
	s_addc_u32 s15, s15, 0
	global_load_dword v233, v241, s[14:15]
	s_add_u32 s14, s14, s46
	s_addc_u32 s15, s15, 0
	s_mov_b32 s48, 1
	s_add_i32 s83, s83, 1
.Lm_bs2:
	s_barrier
	s_add_i32 s77, s77, 1
	v_subrev_u32_e32 v215, 64, v215
	v_lshl_add_u64 v[194:195], v[194:195], 0, s[88:89]
	v_lshl_add_u64 v[196:197], v[196:197], 0, s[68:69]
	v_lshl_add_u64 v[198:199], v[198:199], 0, s[68:69]
.Lm_E1:
	s_add_i32 s4, s77, 1
	s_cmp_ge_u32 s4, s72
	s_cbranch_scc1 .Lm_nd5
	s_add_i32 m0, s74, 0x2000
	s_add_i32 s8, s75, 0x8000
	global_load_lds_dwordx4 v[194:195], off
	s_mov_b32 m0, s8
	s_add_i32 s8, s73, 0x2000
	global_load_lds_dwordx4 v[196:197], off
	s_mov_b32 m0, s8
	s_nop 0
	global_load_lds_dwordx4 v[198:199], off
.Lm_nd5:
	s_cmp_ge_u32 s77, s42
	s_cbranch_scc1 .Lm_a6_slow
	s_cmp_le_u32 s77, s43
	s_cbranch_scc1 .Lm_nm7
	v_add_u32_e32 v239, 64, v215
	v_cmp_gt_i32_e64 s[4:5], 0, v239
	v_cmp_gt_i32_e64 s[6:7], 1, v239
	v_cmp_gt_i32_e64 s[8:9], 2, v239
	v_cmp_gt_i32_e64 s[10:11], 3, v239
	v_cndmask_b32_e64 v68, v68, v211, s[4:5]
	v_cndmask_b32_e64 v69, v69, v211, s[6:7]
	v_cndmask_b32_e64 v70, v70, v211, s[8:9]
	v_cndmask_b32_e64 v71, v71, v211, s[10:11]
	v_cmp_gt_i32_e64 s[4:5], 8, v239
	v_cmp_gt_i32_e64 s[6:7], 9, v239
	v_cmp_gt_i32_e64 s[8:9], 10, v239
	v_cmp_gt_i32_e64 s[10:11], 11, v239
	v_cndmask_b32_e64 v72, v72, v211, s[4:5]
	v_cndmask_b32_e64 v73, v73, v211, s[6:7]
	v_cndmask_b32_e64 v74, v74, v211, s[8:9]
	v_cndmask_b32_e64 v75, v75, v211, s[10:11]
	v_cmp_gt_i32_e64 s[4:5], 16, v239
	v_cmp_gt_i32_e64 s[6:7], 17, v239
	v_cmp_gt_i32_e64 s[8:9], 18, v239
	v_cmp_gt_i32_e64 s[10:11], 19, v239
	v_cndmask_b32_e64 v76, v76, v211, s[4:5]
	v_cndmask_b32_e64 v77, v77, v211, s[6:7]
	v_cndmask_b32_e64 v78, v78, v211, s[8:9]
	v_cndmask_b32_e64 v79, v79, v211, s[10:11]
	v_cmp_gt_i32_e64 s[4:5], 24, v239
	v_cmp_gt_i32_e64 s[6:7], 25, v239
	v_cmp_gt_i32_e64 s[8:9], 26, v239
	v_cmp_gt_i32_e64 s[10:11], 27, v239
	v_cndmask_b32_e64 v80, v80, v211, s[4:5]
	v_cndmask_b32_e64 v81, v81, v211, s[6:7]
	v_cndmask_b32_e64 v82, v82, v211, s[8:9]
	v_cndmask_b32_e64 v83, v83, v211, s[10:11]
	v_cmp_gt_i32_e64 s[4:5], 32, v239
	v_cmp_gt_i32_e64 s[6:7], 33, v239
	v_cmp_gt_i32_e64 s[8:9], 34, v239
	v_cmp_gt_i32_e64 s[10:11], 35, v239
	v_cndmask_b32_e64 v84, v84, v211, s[4:5]
	v_cndmask_b32_e64 v85, v85, v211, s[6:7]
	v_cndmask_b32_e64 v86, v86, v211, s[8:9]
	v_cndmask_b32_e64 v87, v87, v211, s[10:11]
	v_cmp_gt_i32_e64 s[4:5], 40, v239
	v_cmp_gt_i32_e64 s[6:7], 41, v239
	v_cmp_gt_i32_e64 s[8:9], 42, v239
	v_cmp_gt_i32_e64 s[10:11], 43, v239
	v_cndmask_b32_e64 v88, v88, v211, s[4:5]
	v_cndmask_b32_e64 v89, v89, v211, s[6:7]
	v_cndmask_b32_e64 v90, v90, v211, s[8:9]
	v_cndmask_b32_e64 v91, v91, v211, s[10:11]
	v_cmp_gt_i32_e64 s[4:5], 48, v239
	v_cmp_gt_i32_e64 s[6:7], 49, v239
	v_cmp_gt_i32_e64 s[8:9], 50, v239
	v_cmp_gt_i32_e64 s[10:11], 51, v239
	v_cndmask_b32_e64 v92, v92, v211, s[4:5]
	v_cndmask_b32_e64 v93, v93, v211, s[6:7]
	v_cndmask_b32_e64 v94, v94, v211, s[8:9]
	v_cndmask_b32_e64 v95, v95, v211, s[10:11]
	v_cmp_gt_i32_e64 s[4:5], 56, v239
	v_cmp_gt_i32_e64 s[6:7], 57, v239
	v_cmp_gt_i32_e64 s[8:9], 58, v239
	v_cmp_gt_i32_e64 s[10:11], 59, v239
	v_cndmask_b32_e64 v96, v96, v211, s[4:5]
	v_cndmask_b32_e64 v97, v97, v211, s[6:7]
	v_cndmask_b32_e64 v98, v98, v211, s[8:9]
	v_cndmask_b32_e64 v99, v99, v211, s[10:11]
.Lm_nm7:
	ds_read_b128 v[166:169], v200 offset:49152
	ds_read_b128 v[174:177], v200 offset:53248
	ds_read_b128 v[170:173], v201 offset:49152
	ds_read_b128 v[178:181], v201 offset:53248
	ds_read_b128 v[182:185], v202 offset:49152
	ds_read_b128 v[218:221], v202 offset:53248
	ds_read_b128 v[186:189], v203 offset:49152
	ds_read_b128 v[222:225], v203 offset:53248
	v_max3_f32 v239, v68, v69, v70
	v_max3_f32 v235, v84, v85, v86
	v_max3_f32 v239, v239, v71, v72
	v_max3_f32 v235, v235, v87, v88
	v_max3_f32 v239, v239, v73, v74
	v_max3_f32 v235, v235, v89, v90
	v_max3_f32 v239, v239, v75, v76
	v_max3_f32 v235, v235, v91, v92
	v_max3_f32 v239, v239, v77, v78
	v_max3_f32 v235, v235, v93, v94
	v_max3_f32 v239, v239, v79, v80
	v_max3_f32 v235, v235, v95, v96
	v_max3_f32 v239, v239, v81, v82
	v_max3_f32 v235, v235, v97, v98
	v_max3_f32 v239, v239, v83, v99
	v_max_f32_e32 v239, v239, v235
	v_mov_b32_e32 v234, v239
	s_waitcnt lgkmcnt(4)
	v_mfma_f32_32x32x64_f8f6f4 v[124:139], v[166:173], v[100:107], 0
	s_nop 1
	v_permlane32_swap_b32_e32 v239, v234
	v_max_f32_e32 v239, v239, v234
	v_sub_f32_e32 v235, v239, v216
	v_mul_f32_e32 v235, 0x3a93cd3a, v235
	v_cmp_ge_f32_e32 vcc, 2.0, v235
	v_max_f32_e32 v235, v216, v239
	v_sub_f32_e32 v217, v216, v235
	v_mul_f32_e32 v217, 0x3ad53b94, v217
	v_exp_f32_e32 v217, v217
	s_cmp_eq_u64 vcc, exec
	s_cselect_b64 s[4:5], -1, 0
	v_cndmask_b32_e64 v217, v217, 1.0, s[4:5]
	v_cndmask_b32_e64 v216, v235, v216, s[4:5]
	v_cmp_gt_f32_e32 vcc, 1.0, v217
	s_cbranch_vccz .Lm_nr8
	s_and_saveexec_b64 s[6:7], s[0:1]
	ds_write_b32 v214, v217 offset:128
	s_or_b64 exec, exec, s[6:7]
	s_waitcnt lgkmcnt(0)
	ds_read_b128 v[248:251], v213 offset:128
	s_waitcnt lgkmcnt(0)
	v_pk_mul_f32 v[52:53], v[52:53], v[248:249]
	v_pk_mul_f32 v[54:55], v[54:55], v[250:251]
	v_pk_mul_f32 v[36:37], v[36:37], v[248:249]
	v_pk_mul_f32 v[38:39], v[38:39], v[250:251]
	v_pk_mul_f32 v[20:21], v[20:21], v[248:249]
	v_pk_mul_f32 v[22:23], v[22:23], v[250:251]
	v_pk_mul_f32 v[4:5], v[4:5], v[248:249]
	v_pk_mul_f32 v[6:7], v[6:7], v[250:251]
	ds_read_b128 v[248:251], v213 offset:160
	s_waitcnt lgkmcnt(0)
	v_pk_mul_f32 v[56:57], v[56:57], v[248:249]
	v_pk_mul_f32 v[58:59], v[58:59], v[250:251]
	v_pk_mul_f32 v[40:41], v[40:41], v[248:249]
	v_pk_mul_f32 v[42:43], v[42:43], v[250:251]
	v_pk_mul_f32 v[24:25], v[24:25], v[248:249]
	v_pk_mul_f32 v[26:27], v[26:27], v[250:251]
	v_pk_mul_f32 v[8:9], v[8:9], v[248:249]
	v_pk_mul_f32 v[10:11], v[10:11], v[250:251]
	ds_read_b128 v[248:251], v213 offset:192
	s_waitcnt lgkmcnt(0)
	v_pk_mul_f32 v[60:61], v[60:61], v[248:249]
	v_pk_mul_f32 v[62:63], v[62:63], v[250:251]
	v_pk_mul_f32 v[44:45], v[44:45], v[248:249]
	v_pk_mul_f32 v[46:47], v[46:47], v[250:251]
	v_pk_mul_f32 v[28:29], v[28:29], v[248:249]
	v_pk_mul_f32 v[30:31], v[30:31], v[250:251]
	v_pk_mul_f32 v[12:13], v[12:13], v[248:249]
	v_pk_mul_f32 v[14:15], v[14:15], v[250:251]
	ds_read_b128 v[248:251], v213 offset:224
	s_waitcnt lgkmcnt(0)
	v_pk_mul_f32 v[64:65], v[64:65], v[248:249]
	v_pk_mul_f32 v[66:67], v[66:67], v[250:251]
	v_pk_mul_f32 v[48:49], v[48:49], v[248:249]
	v_pk_mul_f32 v[50:51], v[50:51], v[250:251]
	v_pk_mul_f32 v[32:33], v[32:33], v[248:249]
	v_pk_mul_f32 v[34:35], v[34:35], v[250:251]
	v_pk_mul_f32 v[16:17], v[16:17], v[248:249]
	v_pk_mul_f32 v[18:19], v[18:19], v[250:251]
.Lm_nr8:
	v_fmamk_f32 v190, v216, 0xbad53b94, v210
	v_mfma_f32_32x32x64_f8f6f4 v[140:155], v[174:181], v[100:107], 0
	ds_read_b128 v[166:169], v242 offset:8192
	ds_read_b128 v[174:177], v242 offset:12288
	ds_read_b128 v[170:173], v243 offset:8192
	ds_read_b128 v[178:181], v243 offset:12288
	v_pk_fma_f32 v[68:69], v[68:69], s[96:97], v[190:191] op_sel_hi:[1,0,0]
	v_pk_fma_f32 v[84:85], v[84:85], s[96:97], v[190:191] op_sel_hi:[1,0,0]
	v_pk_fma_f32 v[70:71], v[70:71], s[96:97], v[190:191] op_sel_hi:[1,0,0]
	v_pk_fma_f32 v[86:87], v[86:87], s[96:97], v[190:191] op_sel_hi:[1,0,0]
	v_pk_fma_f32 v[72:73], v[72:73], s[96:97], v[190:191] op_sel_hi:[1,0,0]
	v_pk_fma_f32 v[88:89], v[88:89], s[96:97], v[190:191] op_sel_hi:[1,0,0]
	v_pk_fma_f32 v[74:75], v[74:75], s[96:97], v[190:191] op_sel_hi:[1,0,0]
	v_pk_fma_f32 v[90:91], v[90:91], s[96:97], v[190:191] op_sel_hi:[1,0,0]
	s_waitcnt lgkmcnt(4)
	v_mfma_f32_32x32x64_f8f6f4 v[124:139], v[182:189], v[108:115], v[124:139]
	v_pk_fma_f32 v[76:77], v[76:77], s[96:97], v[190:191] op_sel_hi:[1,0,0]
	v_pk_fma_f32 v[92:93], v[92:93], s[96:97], v[190:191] op_sel_hi:[1,0,0]
	v_pk_fma_f32 v[78:79], v[78:79], s[96:97], v[190:191] op_sel_hi:[1,0,0]
	v_pk_fma_f32 v[94:95], v[94:95], s[96:97], v[190:191] op_sel_hi:[1,0,0]
	v_pk_fma_f32 v[80:81], v[80:81], s[96:97], v[190:191] op_sel_hi:[1,0,0]
	v_pk_fma_f32 v[96:97], v[96:97], s[96:97], v[190:191] op_sel_hi:[1,0,0]
	v_pk_fma_f32 v[82:83], v[82:83], s[96:97], v[190:191] op_sel_hi:[1,0,0]
	v_pk_fma_f32 v[98:99], v[98:99], s[96:97], v[190:191] op_sel_hi:[1,0,0]
	v_mfma_f32_32x32x64_f8f6f4 v[140:155], v[218:225], v[108:115], v[140:155]
	v_exp_f32_e32 v68, v68
	v_exp_f32_e32 v69, v69
	v_exp_f32_e32 v70, v70
	v_exp_f32_e32 v71, v71
	v_exp_f32_e32 v72, v72
	v_exp_f32_e32 v73, v73
	v_exp_f32_e32 v74, v74
	v_exp_f32_e32 v75, v75
	s_waitcnt lgkmcnt(0)
	v_mfma_f32_32x32x64_f8f6f4 v[124:139], v[166:173], v[116:123], v[124:139]
	v_exp_f32_e32 v76, v76
	v_exp_f32_e32 v77, v77
	v_exp_f32_e32 v78, v78
	v_exp_f32_e32 v79, v79
	v_exp_f32_e32 v80, v80
	v_exp_f32_e32 v81, v81
	v_exp_f32_e32 v82, v82
	v_exp_f32_e32 v83, v83
	v_mfma_f32_32x32x64_f8f6f4 v[140:155], v[174:181], v[116:123], v[140:155]
.Lm_a6_end:
	s_sub_i32 s5, s77, 1
	s_cmp_ge_u32 s5, s42
	s_cbranch_scc1 .Lm_b9_end
	ds_read_b128 v[166:169], v207 offset:0
	ds_read_b128 v[170:173], v208 offset:0
	ds_read_b128 v[174:177], v207 offset:2048
	ds_read_b128 v[178:181], v208 offset:2048
	ds_read_b128 v[182:185], v207 offset:4096
	ds_read_b128 v[186:189], v208 offset:4096
	ds_read_b128 v[218:221], v207 offset:6144
	ds_read_b128 v[222:225], v208 offset:6144
	v_exp_f32_e32 v84, v84
	v_exp_f32_e32 v85, v85
	v_exp_f32_e32 v86, v86
	v_exp_f32_e32 v87, v87
	v_exp_f32_e32 v88, v88
	v_exp_f32_e32 v89, v89
	v_exp_f32_e32 v90, v90
	v_exp_f32_e32 v91, v91
	v_exp_f32_e32 v92, v92
	v_exp_f32_e32 v93, v93
	v_exp_f32_e32 v94, v94
	v_exp_f32_e32 v95, v95
	v_exp_f32_e32 v96, v96
	v_exp_f32_e32 v97, v97
	v_exp_f32_e32 v98, v98
	v_exp_f32_e32 v99, v99
	v_pk_add_f32 v[192:193], v[68:69], v[70:71]
	v_pk_add_f32 v[234:235], v[84:85], v[86:87]
	v_pk_add_f32 v[192:193], v[72:73], v[192:193]
	v_cvt_pk_fp8_f32 v248, v68, v69
	v_pk_add_f32 v[234:235], v[88:89], v[234:235]
	v_cvt_pk_fp8_f32 v249, v72, v73
	v_pk_add_f32 v[192:193], v[74:75], v[192:193]
	v_cvt_pk_fp8_f32 v250, v76, v77
	v_pk_add_f32 v[234:235], v[90:91], v[234:235]
	v_cvt_pk_fp8_f32 v251, v80, v81
	v_pk_add_f32 v[192:193], v[76:77], v[192:193]
	v_cvt_pk_fp8_f32 v252, v84, v85
	v_pk_add_f32 v[234:235], v[92:93], v[234:235]
	v_cvt_pk_fp8_f32 v253, v88, v89
	v_pk_add_f32 v[192:193], v[78:79], v[192:193]
	v_cvt_pk_fp8_f32 v254, v92, v93
	v_pk_add_f32 v[234:235], v[94:95], v[234:235]
	v_cvt_pk_fp8_f32 v255, v96, v97
	v_pk_add_f32 v[192:193], v[80:81], v[192:193]
	v_pk_add_f32 v[234:235], v[96:97], v[234:235]
	v_pk_add_f32 v[192:193], v[82:83], v[192:193]
	v_pk_add_f32 v[234:235], v[98:99], v[234:235]
	v_pk_add_f32 v[192:193], v[192:193], v[234:235]
	v_cvt_pk_fp8_f32 v248, v70, v71 op_sel:[0,0,1]
	v_cvt_pk_fp8_f32 v249, v74, v75 op_sel:[0,0,1]
	v_cvt_pk_fp8_f32 v250, v78, v79 op_sel:[0,0,1]
	v_cvt_pk_fp8_f32 v251, v82, v83 op_sel:[0,0,1]
	v_add_f32_e32 v239, v192, v193
	v_cvt_pk_fp8_f32 v252, v86, v87 op_sel:[0,0,1]
	v_cvt_pk_fp8_f32 v253, v90, v91 op_sel:[0,0,1]
	v_mov_b32_e32 v235, v239
	v_cvt_pk_fp8_f32 v254, v94, v95 op_sel:[0,0,1]
	v_cvt_pk_fp8_f32 v255, v98, v99 op_sel:[0,0,1]
	v_permlane32_swap_b32_e32 v239, v235
	v_add_f32_e32 v239, v239, v235
	v_fma_f32 v2, v2, v217, v239
	s_nop 1
	s_waitcnt lgkmcnt(4)
	v_mfma_f32_32x32x64_f8f6f4 v[52:67], v[248:255], v[166:173], v[52:67]
	v_mfma_f32_32x32x64_f8f6f4 v[36:51], v[248:255], v[174:181], v[36:51]
	s_waitcnt lgkmcnt(0)
	v_mfma_f32_32x32x64_f8f6f4 v[20:35], v[248:255], v[182:189], v[20:35]
	v_mfma_f32_32x32x64_f8f6f4 v[4:19], v[248:255], v[218:225], v[4:19]
.Lm_b9_end:
	s_waitcnt vmcnt(0) lgkmcnt(0)
	s_cmp_eq_u32 s48, 0
	s_cbranch_scc1 .Lm_bi10
	v_pk_mul_f32 v[226:227], v[226:227], s[50:51]
	v_pk_mul_f32 v[228:229], v[228:229], s[50:51]
	v_pk_mul_f32 v[230:231], v[230:231], s[50:51]
	v_pk_mul_f32 v[232:233], v[232:233], s[50:51]
	v_med3_f32 v226, v226, s33, v212
	v_med3_f32 v227, v227, s33, v212
	v_med3_f32 v228, v228, s33, v212
	v_med3_f32 v229, v229, s33, v212
	v_med3_f32 v230, v230, s33, v212
	v_med3_f32 v231, v231, s33, v212
	v_med3_f32 v232, v232, s33, v212
	v_med3_f32 v233, v233, s33, v212
	v_cvt_pk_fp8_f32 v244, v226, v227
	v_cvt_pk_fp8_f32 v245, v230, v231
	v_cvt_pk_fp8_f32 v244, v228, v229 op_sel:[0,0,1]
	v_cvt_pk_fp8_f32 v245, v232, v233 op_sel:[0,0,1]
	global_load_dword v226, v241, s[14:15]
	s_add_u32 s14, s14, s46
	s_addc_u32 s15, s15, 0
	global_load_dword v227, v241, s[14:15]
	s_add_u32 s14, s14, s46
	s_addc_u32 s15, s15, 0
	global_load_dword v228, v241, s[14:15]
	s_add_u32 s14, s14, s46
	s_addc_u32 s15, s15, 0
	global_load_dword v229, v241, s[14:15]
	s_add_u32 s14, s14, s46
	s_addc_u32 s15, s15, 0
	global_load_dword v230, v241, s[14:15]
	s_add_u32 s14, s14, s46
	s_addc_u32 s15, s15, 0
	global_load_dword v231, v241, s[14:15]
	s_add_u32 s14, s14, s46
	s_addc_u32 s15, s15, 0
	global_load_dword v232, v241, s[14:15]
	s_add_u32 s14, s14, s46
	s_addc_u32 s15, s15, 0
	global_load_dword v233, v241, s[14:15]
	s_add_u32 s14, s14, s46
	s_addc_u32 s15, s15, 0

.Lm_E2:
	s_add_i32 s4, s77, 1
	s_cmp_ge_u32 s4, s72
	s_cbranch_scc1 .Lm_nd11
	s_add_i32 m0, s74, 0x6000
	s_add_i32 s8, s75, 0xa000
	global_load_lds_dwordx4 v[194:195], off
	s_mov_b32 m0, s8
	s_add_i32 s8, s73, 0x6000
	global_load_lds_dwordx4 v[196:197], off
	s_mov_b32 m0, s8
	s_nop 0
	global_load_lds_dwordx4 v[198:199], off
.Lm_nd11:
	s_cmp_ge_u32 s77, s42
	s_cbranch_scc1 .Lm_a12_slow
	s_cmp_le_u32 s77, s43
	s_cbranch_scc1 .Lm_nm13
	v_add_u32_e32 v239, 64, v215
	v_cmp_gt_i32_e64 s[4:5], 0, v239
	v_cmp_gt_i32_e64 s[6:7], 1, v239
	v_cmp_gt_i32_e64 s[8:9], 2, v239
	v_cmp_gt_i32_e64 s[10:11], 3, v239
	v_cndmask_b32_e64 v124, v124, v211, s[4:5]
	v_cndmask_b32_e64 v125, v125, v211, s[6:7]
	v_cndmask_b32_e64 v126, v126, v211, s[8:9]
	v_cndmask_b32_e64 v127, v127, v211, s[10:11]
	v_cmp_gt_i32_e64 s[4:5], 8, v239
	v_cmp_gt_i32_e64 s[6:7], 9, v239
	v_cmp_gt_i32_e64 s[8:9], 10, v239
	v_cmp_gt_i32_e64 s[10:11], 11, v239
	v_cndmask_b32_e64 v128, v128, v211, s[4:5]
	v_cndmask_b32_e64 v129, v129, v211, s[6:7]
	v_cndmask_b32_e64 v130, v130, v211, s[8:9]
	v_cndmask_b32_e64 v131, v131, v211, s[10:11]
	v_cmp_gt_i32_e64 s[4:5], 16, v239
	v_cmp_gt_i32_e64 s[6:7], 17, v239
	v_cmp_gt_i32_e64 s[8:9], 18, v239
	v_cmp_gt_i32_e64 s[10:11], 19, v239
	v_cndmask_b32_e64 v132, v132, v211, s[4:5]
	v_cndmask_b32_e64 v133, v133, v211, s[6:7]
	v_cndmask_b32_e64 v134, v134, v211, s[8:9]
	v_cndmask_b32_e64 v135, v135, v211, s[10:11]
	v_cmp_gt_i32_e64 s[4:5], 24, v239
	v_cmp_gt_i32_e64 s[6:7], 25, v239
	v_cmp_gt_i32_e64 s[8:9], 26, v239
	v_cmp_gt_i32_e64 s[10:11], 27, v239
	v_cndmask_b32_e64 v136, v136, v211, s[4:5]
	v_cndmask_b32_e64 v137, v137, v211, s[6:7]
	v_cndmask_b32_e64 v138, v138, v211, s[8:9]
	v_cndmask_b32_e64 v139, v139, v211, s[10:11]
	v_cmp_gt_i32_e64 s[4:5], 32, v239
	v_cmp_gt_i32_e64 s[6:7], 33, v239
	v_cmp_gt_i32_e64 s[8:9], 34, v239
	v_cmp_gt_i32_e64 s[10:11], 35, v239
	v_cndmask_b32_e64 v140, v140, v211, s[4:5]
	v_cndmask_b32_e64 v141, v141, v211, s[6:7]
	v_cndmask_b32_e64 v142, v142, v211, s[8:9]
	v_cndmask_b32_e64 v143, v143, v211, s[10:11]
	v_cmp_gt_i32_e64 s[4:5], 40, v239
	v_cmp_gt_i32_e64 s[6:7], 41, v239
	v_cmp_gt_i32_e64 s[8:9], 42, v239
	v_cmp_gt_i32_e64 s[10:11], 43, v239
	v_cndmask_b32_e64 v144, v144, v211, s[4:5]
	v_cndmask_b32_e64 v145, v145, v211, s[6:7]
	v_cndmask_b32_e64 v146, v146, v211, s[8:9]
	v_cndmask_b32_e64 v147, v147, v211, s[10:11]
	v_cmp_gt_i32_e64 s[4:5], 48, v239
	v_cmp_gt_i32_e64 s[6:7], 49, v239
	v_cmp_gt_i32_e64 s[8:9], 50, v239
	v_cmp_gt_i32_e64 s[10:11], 51, v239
	v_cndmask_b32_e64 v148, v148, v211, s[4:5]
	v_cndmask_b32_e64 v149, v149, v211, s[6:7]
	v_cndmask_b32_e64 v150, v150, v211, s[8:9]
	v_cndmask_b32_e64 v151, v151, v211, s[10:11]
	v_cmp_gt_i32_e64 s[4:5], 56, v239
	v_cmp_gt_i32_e64 s[6:7], 57, v239
	v_cmp_gt_i32_e64 s[8:9], 58, v239
	v_cmp_gt_i32_e64 s[10:11], 59, v239
	v_cndmask_b32_e64 v152, v152, v211, s[4:5]
	v_cndmask_b32_e64 v153, v153, v211, s[6:7]
	v_cndmask_b32_e64 v154, v154, v211, s[8:9]
	v_cndmask_b32_e64 v155, v155, v211, s[10:11]
.Lm_nm13:
	ds_read_b128 v[166:169], v200 offset:40960
	ds_read_b128 v[174:177], v200 offset:45056
	ds_read_b128 v[170:173], v201 offset:40960
	ds_read_b128 v[178:181], v201 offset:45056
	ds_read_b128 v[182:185], v202 offset:40960
	ds_read_b128 v[218:221], v202 offset:45056
	ds_read_b128 v[186:189], v203 offset:40960
	ds_read_b128 v[222:225], v203 offset:45056
	v_max3_f32 v239, v124, v125, v126
	v_max3_f32 v235, v140, v141, v142
	v_max3_f32 v239, v239, v127, v128
	v_max3_f32 v235, v235, v143, v144
	v_max3_f32 v239, v239, v129, v130
	v_max3_f32 v235, v235, v145, v146
	v_max3_f32 v239, v239, v131, v132
	v_max3_f32 v235, v235, v147, v148
	v_max3_f32 v239, v239, v133, v134
	v_max3_f32 v235, v235, v149, v150
	v_max3_f32 v239, v239, v135, v136
	v_max3_f32 v235, v235, v151, v152
	v_max3_f32 v239, v239, v137, v138
	v_max3_f32 v235, v235, v153, v154
	v_max3_f32 v239, v239, v139, v155
	v_max_f32_e32 v239, v239, v235
	v_mov_b32_e32 v234, v239
	s_waitcnt lgkmcnt(4)
	v_mfma_f32_32x32x64_f8f6f4 v[68:83], v[166:173], v[100:107], 0
	s_nop 1
	v_permlane32_swap_b32_e32 v239, v234
	v_max_f32_e32 v239, v239, v234
	v_sub_f32_e32 v235, v239, v216
	v_mul_f32_e32 v235, 0x3a93cd3a, v235
	v_cmp_ge_f32_e32 vcc, 2.0, v235
	v_max_f32_e32 v235, v216, v239
	v_sub_f32_e32 v217, v216, v235
	v_mul_f32_e32 v217, 0x3ad53b94, v217
	v_exp_f32_e32 v217, v217
	s_cmp_eq_u64 vcc, exec
	s_cselect_b64 s[4:5], -1, 0
	v_cndmask_b32_e64 v217, v217, 1.0, s[4:5]
	v_cndmask_b32_e64 v216, v235, v216, s[4:5]
	v_cmp_gt_f32_e32 vcc, 1.0, v217
	s_cbranch_vccz .Lm_nr14
	s_and_saveexec_b64 s[6:7], s[0:1]
	ds_write_b32 v214, v217 offset:128
	s_or_b64 exec, exec, s[6:7]
	s_waitcnt lgkmcnt(0)
	ds_read_b128 v[248:251], v213 offset:128
	s_waitcnt lgkmcnt(0)
	v_pk_mul_f32 v[52:53], v[52:53], v[248:249]
	v_pk_mul_f32 v[54:55], v[54:55], v[250:251]
	v_pk_mul_f32 v[36:37], v[36:37], v[248:249]
	v_pk_mul_f32 v[38:39], v[38:39], v[250:251]
	v_pk_mul_f32 v[20:21], v[20:21], v[248:249]
	v_pk_mul_f32 v[22:23], v[22:23], v[250:251]
	v_pk_mul_f32 v[4:5], v[4:5], v[248:249]
	v_pk_mul_f32 v[6:7], v[6:7], v[250:251]
	ds_read_b128 v[248:251], v213 offset:160
	s_waitcnt lgkmcnt(0)
	v_pk_mul_f32 v[56:57], v[56:57], v[248:249]
	v_pk_mul_f32 v[58:59], v[58:59], v[250:251]
	v_pk_mul_f32 v[40:41], v[40:41], v[248:249]
	v_pk_mul_f32 v[42:43], v[42:43], v[250:251]
	v_pk_mul_f32 v[24:25], v[24:25], v[248:249]
	v_pk_mul_f32 v[26:27], v[26:27], v[250:251]
	v_pk_mul_f32 v[8:9], v[8:9], v[248:249]
	v_pk_mul_f32 v[10:11], v[10:11], v[250:251]
	ds_read_b128 v[248:251], v213 offset:192
	s_waitcnt lgkmcnt(0)
	v_pk_mul_f32 v[60:61], v[60:61], v[248:249]
	v_pk_mul_f32 v[62:63], v[62:63], v[250:251]
	v_pk_mul_f32 v[44:45], v[44:45], v[248:249]
	v_pk_mul_f32 v[46:47], v[46:47], v[250:251]
	v_pk_mul_f32 v[28:29], v[28:29], v[248:249]
	v_pk_mul_f32 v[30:31], v[30:31], v[250:251]
	v_pk_mul_f32 v[12:13], v[12:13], v[248:249]
	v_pk_mul_f32 v[14:15], v[14:15], v[250:251]
	ds_read_b128 v[248:251], v213 offset:224
	s_waitcnt lgkmcnt(0)
	v_pk_mul_f32 v[64:65], v[64:65], v[248:249]
	v_pk_mul_f32 v[66:67], v[66:67], v[250:251]
	v_pk_mul_f32 v[48:49], v[48:49], v[248:249]
	v_pk_mul_f32 v[50:51], v[50:51], v[250:251]
	v_pk_mul_f32 v[32:33], v[32:33], v[248:249]
	v_pk_mul_f32 v[34:35], v[34:35], v[250:251]
	v_pk_mul_f32 v[16:17], v[16:17], v[248:249]
	v_pk_mul_f32 v[18:19], v[18:19], v[250:251]
.Lm_nr14:
	v_fmamk_f32 v190, v216, 0xbad53b94, v210
	v_mfma_f32_32x32x64_f8f6f4 v[84:99], v[174:181], v[100:107], 0
	ds_read_b128 v[166:169], v242 offset:32768
	ds_read_b128 v[174:177], v242 offset:36864
	ds_read_b128 v[170:173], v243 offset:32768
	ds_read_b128 v[178:181], v243 offset:36864
	v_pk_fma_f32 v[124:125], v[124:125], s[96:97], v[190:191] op_sel_hi:[1,0,0]
	v_pk_fma_f32 v[140:141], v[140:141], s[96:97], v[190:191] op_sel_hi:[1,0,0]
	v_pk_fma_f32 v[126:127], v[126:127], s[96:97], v[190:191] op_sel_hi:[1,0,0]
	v_pk_fma_f32 v[142:143], v[142:143], s[96:97], v[190:191] op_sel_hi:[1,0,0]
	v_pk_fma_f32 v[128:129], v[128:129], s[96:97], v[190:191] op_sel_hi:[1,0,0]
	v_pk_fma_f32 v[144:145], v[144:145], s[96:97], v[190:191] op_sel_hi:[1,0,0]
	v_pk_fma_f32 v[130:131], v[130:131], s[96:97], v[190:191] op_sel_hi:[1,0,0]
	v_pk_fma_f32 v[146:147], v[146:147], s[96:97], v[190:191] op_sel_hi:[1,0,0]
	s_waitcnt lgkmcnt(4)
	v_mfma_f32_32x32x64_f8f6f4 v[68:83], v[182:189], v[108:115], v[68:83]
	v_pk_fma_f32 v[132:133], v[132:133], s[96:97], v[190:191] op_sel_hi:[1,0,0]
	v_pk_fma_f32 v[148:149], v[148:149], s[96:97], v[190:191] op_sel_hi:[1,0,0]
	v_pk_fma_f32 v[134:135], v[134:135], s[96:97], v[190:191] op_sel_hi:[1,0,0]
	v_pk_fma_f32 v[150:151], v[150:151], s[96:97], v[190:191] op_sel_hi:[1,0,0]
	v_pk_fma_f32 v[136:137], v[136:137], s[96:97], v[190:191] op_sel_hi:[1,0,0]
	v_pk_fma_f32 v[152:153], v[152:153], s[96:97], v[190:191] op_sel_hi:[1,0,0]
	v_pk_fma_f32 v[138:139], v[138:139], s[96:97], v[190:191] op_sel_hi:[1,0,0]
	v_pk_fma_f32 v[154:155], v[154:155], s[96:97], v[190:191] op_sel_hi:[1,0,0]
	v_mfma_f32_32x32x64_f8f6f4 v[84:99], v[218:225], v[108:115], v[84:99]
	v_exp_f32_e32 v124, v124
	v_exp_f32_e32 v125, v125
	v_exp_f32_e32 v126, v126
	v_exp_f32_e32 v127, v127
	v_exp_f32_e32 v128, v128
	v_exp_f32_e32 v129, v129
	v_exp_f32_e32 v130, v130
	v_exp_f32_e32 v131, v131
	s_waitcnt lgkmcnt(0)
	v_mfma_f32_32x32x64_f8f6f4 v[68:83], v[166:173], v[116:123], v[68:83]
	v_exp_f32_e32 v132, v132
	v_exp_f32_e32 v133, v133
	v_exp_f32_e32 v134, v134
	v_exp_f32_e32 v135, v135
	v_exp_f32_e32 v136, v136
	v_exp_f32_e32 v137, v137
	v_exp_f32_e32 v138, v138
	v_exp_f32_e32 v139, v139
	v_mfma_f32_32x32x64_f8f6f4 v[84:99], v[174:181], v[116:123], v[84:99]
.Lm_a12_end:
	s_sub_i32 s5, s77, 1
	s_cmp_ge_u32 s5, s42
	s_cbranch_scc1 .Lm_b15_end
	ds_read_b128 v[166:169], v207 offset:16384
	ds_read_b128 v[170:173], v208 offset:16384
	ds_read_b128 v[174:177], v207 offset:18432
	ds_read_b128 v[178:181], v208 offset:18432
	ds_read_b128 v[182:185], v207 offset:20480
	ds_read_b128 v[186:189], v208 offset:20480
	ds_read_b128 v[218:221], v207 offset:22528
	ds_read_b128 v[222:225], v208 offset:22528
	v_exp_f32_e32 v140, v140
	v_exp_f32_e32 v141, v141
	v_exp_f32_e32 v142, v142
	v_exp_f32_e32 v143, v143
	v_exp_f32_e32 v144, v144
	v_exp_f32_e32 v145, v145
	v_exp_f32_e32 v146, v146
	v_exp_f32_e32 v147, v147
	v_exp_f32_e32 v148, v148
	v_exp_f32_e32 v149, v149
	v_exp_f32_e32 v150, v150
	v_exp_f32_e32 v151, v151
	v_exp_f32_e32 v152, v152
	v_exp_f32_e32 v153, v153
	v_exp_f32_e32 v154, v154
	v_exp_f32_e32 v155, v155
	v_pk_add_f32 v[192:193], v[124:125], v[126:127]
	v_pk_add_f32 v[234:235], v[140:141], v[142:143]
	v_pk_add_f32 v[192:193], v[128:129], v[192:193]
	v_cvt_pk_fp8_f32 v248, v124, v125
	v_pk_add_f32 v[234:235], v[144:145], v[234:235]
	v_cvt_pk_fp8_f32 v249, v128, v129
	v_pk_add_f32 v[192:193], v[130:131], v[192:193]
	v_cvt_pk_fp8_f32 v250, v132, v133
	v_pk_add_f32 v[234:235], v[146:147], v[234:235]
	v_cvt_pk_fp8_f32 v251, v136, v137
	v_pk_add_f32 v[192:193], v[132:133], v[192:193]
	v_cvt_pk_fp8_f32 v252, v140, v141
	v_pk_add_f32 v[234:235], v[148:149], v[234:235]
	v_cvt_pk_fp8_f32 v253, v144, v145
	v_pk_add_f32 v[192:193], v[134:135], v[192:193]
	v_cvt_pk_fp8_f32 v254, v148, v149
	v_pk_add_f32 v[234:235], v[150:151], v[234:235]
	v_cvt_pk_fp8_f32 v255, v152, v153
	v_pk_add_f32 v[192:193], v[136:137], v[192:193]
	v_pk_add_f32 v[234:235], v[152:153], v[234:235]
	v_pk_add_f32 v[192:193], v[138:139], v[192:193]
	v_pk_add_f32 v[234:235], v[154:155], v[234:235]
	v_pk_add_f32 v[192:193], v[192:193], v[234:235]
	v_cvt_pk_fp8_f32 v248, v126, v127 op_sel:[0,0,1]
	v_cvt_pk_fp8_f32 v249, v130, v131 op_sel:[0,0,1]
	v_cvt_pk_fp8_f32 v250, v134, v135 op_sel:[0,0,1]
	v_cvt_pk_fp8_f32 v251, v138, v139 op_sel:[0,0,1]
	v_add_f32_e32 v239, v192, v193
	v_cvt_pk_fp8_f32 v252, v142, v143 op_sel:[0,0,1]
	v_cvt_pk_fp8_f32 v253, v146, v147 op_sel:[0,0,1]
	v_mov_b32_e32 v235, v239
	v_cvt_pk_fp8_f32 v254, v150, v151 op_sel:[0,0,1]
	v_cvt_pk_fp8_f32 v255, v154, v155 op_sel:[0,0,1]
	v_permlane32_swap_b32_e32 v239, v235
	v_add_f32_e32 v239, v239, v235
	v_fma_f32 v2, v2, v217, v239
	s_nop 1
	s_waitcnt lgkmcnt(4)
	v_mfma_f32_32x32x64_f8f6f4 v[52:67], v[248:255], v[166:173], v[52:67]
	v_mfma_f32_32x32x64_f8f6f4 v[36:51], v[248:255], v[174:181], v[36:51]
	s_waitcnt lgkmcnt(0)
	v_mfma_f32_32x32x64_f8f6f4 v[20:35], v[248:255], v[182:189], v[20:35]
	v_mfma_f32_32x32x64_f8f6f4 v[4:19], v[248:255], v[218:225], v[4:19]
.Lm_b15_end:
	s_waitcnt vmcnt(0) lgkmcnt(0)
	s_cmp_eq_u32 s48, 0
	s_cbranch_scc1 .Lm_bf17
	v_pk_mul_f32 v[226:227], v[226:227], s[50:51]
	v_pk_mul_f32 v[228:229], v[228:229], s[50:51]
	v_pk_mul_f32 v[230:231], v[230:231], s[50:51]
	v_pk_mul_f32 v[232:233], v[232:233], s[50:51]
	v_med3_f32 v226, v226, s33, v212
	v_med3_f32 v227, v227, s33, v212
	v_med3_f32 v228, v228, s33, v212
	v_med3_f32 v229, v229, s33, v212
	v_med3_f32 v230, v230, s33, v212
	v_med3_f32 v231, v231, s33, v212
	v_med3_f32 v232, v232, s33, v212
	v_med3_f32 v233, v233, s33, v212
	v_cvt_pk_fp8_f32 v246, v226, v227
	v_cvt_pk_fp8_f32 v247, v230, v231
	v_cvt_pk_fp8_f32 v246, v228, v229 op_sel:[0,0,1]
	v_cvt_pk_fp8_f32 v247, v232, v233 op_sel:[0,0,1]
	global_store_dwordx4 v240, v[244:247], s[44:45]
	s_mov_b32 s48, 0

.Lm_E3:
	s_add_i32 s4, s77, 1
	s_cmp_ge_u32 s4, s72
	s_cbranch_scc1 .Lm_nd19
	s_add_i32 m0, s74, 0x0
	s_add_i32 s8, s75, 0x0
	global_load_lds_dwordx4 v[194:195], off
	s_mov_b32 m0, s8
	s_add_i32 s8, s73, 0x0
	global_load_lds_dwordx4 v[196:197], off
	s_mov_b32 m0, s8
	s_nop 0
	global_load_lds_dwordx4 v[198:199], off

.Lm_nm21:
	ds_read_b128 v[166:169], v200 offset:57344
	ds_read_b128 v[174:177], v200 offset:61440
	ds_read_b128 v[170:173], v201 offset:57344
	ds_read_b128 v[178:181], v201 offset:61440
	ds_read_b128 v[182:185], v202 offset:57344
	ds_read_b128 v[218:221], v202 offset:61440
	ds_read_b128 v[186:189], v203 offset:57344
	ds_read_b128 v[222:225], v203 offset:61440
	v_max3_f32 v239, v68, v69, v70
	v_max3_f32 v235, v84, v85, v86
	v_max3_f32 v239, v239, v71, v72
	v_max3_f32 v235, v235, v87, v88
	v_max3_f32 v239, v239, v73, v74
	v_max3_f32 v235, v235, v89, v90
	v_max3_f32 v239, v239, v75, v76
	v_max3_f32 v235, v235, v91, v92
	v_max3_f32 v239, v239, v77, v78
	v_max3_f32 v235, v235, v93, v94
	v_max3_f32 v239, v239, v79, v80
	v_max3_f32 v235, v235, v95, v96
	v_max3_f32 v239, v239, v81, v82
	v_max3_f32 v235, v235, v97, v98
	v_max3_f32 v239, v239, v83, v99
	v_max_f32_e32 v239, v239, v235
	v_mov_b32_e32 v234, v239
	s_waitcnt lgkmcnt(4)
	v_mfma_f32_32x32x64_f8f6f4 v[124:139], v[166:173], v[100:107], 0
	s_nop 1
	v_permlane32_swap_b32_e32 v239, v234
	v_max_f32_e32 v239, v239, v234
	v_sub_f32_e32 v235, v239, v216
	v_mul_f32_e32 v235, 0x3a93cd3a, v235
	v_cmp_ge_f32_e32 vcc, 2.0, v235
	v_max_f32_e32 v235, v216, v239
	v_sub_f32_e32 v217, v216, v235
	v_mul_f32_e32 v217, 0x3ad53b94, v217
	v_exp_f32_e32 v217, v217
	s_cmp_eq_u64 vcc, exec
	s_cselect_b64 s[4:5], -1, 0
	v_cndmask_b32_e64 v217, v217, 1.0, s[4:5]
	v_cndmask_b32_e64 v216, v235, v216, s[4:5]
	v_cmp_gt_f32_e32 vcc, 1.0, v217
	s_cbranch_vccz .Lm_nr22
	s_and_saveexec_b64 s[6:7], s[0:1]
	ds_write_b32 v214, v217 offset:128
	s_or_b64 exec, exec, s[6:7]
	s_waitcnt lgkmcnt(0)
	ds_read_b128 v[248:251], v213 offset:128
	s_waitcnt lgkmcnt(0)
	v_pk_mul_f32 v[52:53], v[52:53], v[248:249]
	v_pk_mul_f32 v[54:55], v[54:55], v[250:251]
	v_pk_mul_f32 v[36:37], v[36:37], v[248:249]
	v_pk_mul_f32 v[38:39], v[38:39], v[250:251]
	v_pk_mul_f32 v[20:21], v[20:21], v[248:249]
	v_pk_mul_f32 v[22:23], v[22:23], v[250:251]
	v_pk_mul_f32 v[4:5], v[4:5], v[248:249]
	v_pk_mul_f32 v[6:7], v[6:7], v[250:251]
	ds_read_b128 v[248:251], v213 offset:160
	s_waitcnt lgkmcnt(0)
	v_pk_mul_f32 v[56:57], v[56:57], v[248:249]
	v_pk_mul_f32 v[58:59], v[58:59], v[250:251]
	v_pk_mul_f32 v[40:41], v[40:41], v[248:249]
	v_pk_mul_f32 v[42:43], v[42:43], v[250:251]
	v_pk_mul_f32 v[24:25], v[24:25], v[248:249]
	v_pk_mul_f32 v[26:27], v[26:27], v[250:251]
	v_pk_mul_f32 v[8:9], v[8:9], v[248:249]
	v_pk_mul_f32 v[10:11], v[10:11], v[250:251]
	ds_read_b128 v[248:251], v213 offset:192
	s_waitcnt lgkmcnt(0)
	v_pk_mul_f32 v[60:61], v[60:61], v[248:249]
	v_pk_mul_f32 v[62:63], v[62:63], v[250:251]
	v_pk_mul_f32 v[44:45], v[44:45], v[248:249]
	v_pk_mul_f32 v[46:47], v[46:47], v[250:251]
	v_pk_mul_f32 v[28:29], v[28:29], v[248:249]
	v_pk_mul_f32 v[30:31], v[30:31], v[250:251]
	v_pk_mul_f32 v[12:13], v[12:13], v[248:249]
	v_pk_mul_f32 v[14:15], v[14:15], v[250:251]
	ds_read_b128 v[248:251], v213 offset:224
	s_waitcnt lgkmcnt(0)
	v_pk_mul_f32 v[64:65], v[64:65], v[248:249]
	v_pk_mul_f32 v[66:67], v[66:67], v[250:251]
	v_pk_mul_f32 v[48:49], v[48:49], v[248:249]
	v_pk_mul_f32 v[50:51], v[50:51], v[250:251]
	v_pk_mul_f32 v[32:33], v[32:33], v[248:249]
	v_pk_mul_f32 v[34:35], v[34:35], v[250:251]
	v_pk_mul_f32 v[16:17], v[16:17], v[248:249]
	v_pk_mul_f32 v[18:19], v[18:19], v[250:251]
.Lm_nr22:
	v_fmamk_f32 v190, v216, 0xbad53b94, v210
	v_mfma_f32_32x32x64_f8f6f4 v[140:155], v[174:181], v[100:107], 0
	ds_read_b128 v[166:169], v242 offset:40960
	ds_read_b128 v[174:177], v242 offset:45056
	ds_read_b128 v[170:173], v243 offset:40960
	ds_read_b128 v[178:181], v243 offset:45056
	v_pk_fma_f32 v[68:69], v[68:69], s[96:97], v[190:191] op_sel_hi:[1,0,0]
	v_pk_fma_f32 v[84:85], v[84:85], s[96:97], v[190:191] op_sel_hi:[1,0,0]
	v_pk_fma_f32 v[70:71], v[70:71], s[96:97], v[190:191] op_sel_hi:[1,0,0]
	v_pk_fma_f32 v[86:87], v[86:87], s[96:97], v[190:191] op_sel_hi:[1,0,0]
	v_pk_fma_f32 v[72:73], v[72:73], s[96:97], v[190:191] op_sel_hi:[1,0,0]
	v_pk_fma_f32 v[88:89], v[88:89], s[96:97], v[190:191] op_sel_hi:[1,0,0]
	v_pk_fma_f32 v[74:75], v[74:75], s[96:97], v[190:191] op_sel_hi:[1,0,0]
	v_pk_fma_f32 v[90:91], v[90:91], s[96:97], v[190:191] op_sel_hi:[1,0,0]
	s_waitcnt lgkmcnt(4)
	v_mfma_f32_32x32x64_f8f6f4 v[124:139], v[182:189], v[108:115], v[124:139]
	v_pk_fma_f32 v[76:77], v[76:77], s[96:97], v[190:191] op_sel_hi:[1,0,0]
	v_pk_fma_f32 v[92:93], v[92:93], s[96:97], v[190:191] op_sel_hi:[1,0,0]
	v_pk_fma_f32 v[78:79], v[78:79], s[96:97], v[190:191] op_sel_hi:[1,0,0]
	v_pk_fma_f32 v[94:95], v[94:95], s[96:97], v[190:191] op_sel_hi:[1,0,0]
	v_pk_fma_f32 v[80:81], v[80:81], s[96:97], v[190:191] op_sel_hi:[1,0,0]
	v_pk_fma_f32 v[96:97], v[96:97], s[96:97], v[190:191] op_sel_hi:[1,0,0]
	v_pk_fma_f32 v[82:83], v[82:83], s[96:97], v[190:191] op_sel_hi:[1,0,0]
	v_pk_fma_f32 v[98:99], v[98:99], s[96:97], v[190:191] op_sel_hi:[1,0,0]
	v_mfma_f32_32x32x64_f8f6f4 v[140:155], v[218:225], v[108:115], v[140:155]
	v_exp_f32_e32 v68, v68
	v_exp_f32_e32 v69, v69
	v_exp_f32_e32 v70, v70
	v_exp_f32_e32 v71, v71
	v_exp_f32_e32 v72, v72
	v_exp_f32_e32 v73, v73
	v_exp_f32_e32 v74, v74
	v_exp_f32_e32 v75, v75
	s_waitcnt lgkmcnt(0)
	v_mfma_f32_32x32x64_f8f6f4 v[124:139], v[166:173], v[116:123], v[124:139]
	v_exp_f32_e32 v76, v76
	v_exp_f32_e32 v77, v77
	v_exp_f32_e32 v78, v78
	v_exp_f32_e32 v79, v79
	v_exp_f32_e32 v80, v80
	v_exp_f32_e32 v81, v81
	v_exp_f32_e32 v82, v82
	v_exp_f32_e32 v83, v83
	v_mfma_f32_32x32x64_f8f6f4 v[140:155], v[174:181], v[116:123], v[140:155]
.Lm_a20_end:
	s_sub_i32 s5, s77, 1
	s_cmp_ge_u32 s5, s42
	s_cbranch_scc1 .Lm_b23_end
	ds_read_b128 v[166:169], v207 offset:8192
	ds_read_b128 v[170:173], v208 offset:8192
	ds_read_b128 v[174:177], v207 offset:10240
	ds_read_b128 v[178:181], v208 offset:10240
	ds_read_b128 v[182:185], v207 offset:12288
	ds_read_b128 v[186:189], v208 offset:12288
	ds_read_b128 v[218:221], v207 offset:14336
	ds_read_b128 v[222:225], v208 offset:14336
	v_exp_f32_e32 v84, v84
	v_exp_f32_e32 v85, v85
	v_exp_f32_e32 v86, v86
	v_exp_f32_e32 v87, v87
	v_exp_f32_e32 v88, v88
	v_exp_f32_e32 v89, v89
	v_exp_f32_e32 v90, v90
	v_exp_f32_e32 v91, v91
	v_exp_f32_e32 v92, v92
	v_exp_f32_e32 v93, v93
	v_exp_f32_e32 v94, v94
	v_exp_f32_e32 v95, v95
	v_exp_f32_e32 v96, v96
	v_exp_f32_e32 v97, v97
	v_exp_f32_e32 v98, v98
	v_exp_f32_e32 v99, v99
	v_pk_add_f32 v[192:193], v[68:69], v[70:71]
	v_pk_add_f32 v[234:235], v[84:85], v[86:87]
	v_pk_add_f32 v[192:193], v[72:73], v[192:193]
	v_cvt_pk_fp8_f32 v248, v68, v69
	v_pk_add_f32 v[234:235], v[88:89], v[234:235]
	v_cvt_pk_fp8_f32 v249, v72, v73
	v_pk_add_f32 v[192:193], v[74:75], v[192:193]
	v_cvt_pk_fp8_f32 v250, v76, v77
	v_pk_add_f32 v[234:235], v[90:91], v[234:235]
	v_cvt_pk_fp8_f32 v251, v80, v81
	v_pk_add_f32 v[192:193], v[76:77], v[192:193]
	v_cvt_pk_fp8_f32 v252, v84, v85
	v_pk_add_f32 v[234:235], v[92:93], v[234:235]
	v_cvt_pk_fp8_f32 v253, v88, v89
	v_pk_add_f32 v[192:193], v[78:79], v[192:193]
	v_cvt_pk_fp8_f32 v254, v92, v93
	v_pk_add_f32 v[234:235], v[94:95], v[234:235]
	v_cvt_pk_fp8_f32 v255, v96, v97
	v_pk_add_f32 v[192:193], v[80:81], v[192:193]
	v_pk_add_f32 v[234:235], v[96:97], v[234:235]
	v_pk_add_f32 v[192:193], v[82:83], v[192:193]
	v_pk_add_f32 v[234:235], v[98:99], v[234:235]
	v_pk_add_f32 v[192:193], v[192:193], v[234:235]
	v_cvt_pk_fp8_f32 v248, v70, v71 op_sel:[0,0,1]
	v_cvt_pk_fp8_f32 v249, v74, v75 op_sel:[0,0,1]
	v_cvt_pk_fp8_f32 v250, v78, v79 op_sel:[0,0,1]
	v_cvt_pk_fp8_f32 v251, v82, v83 op_sel:[0,0,1]
	v_add_f32_e32 v239, v192, v193
	v_cvt_pk_fp8_f32 v252, v86, v87 op_sel:[0,0,1]
	v_cvt_pk_fp8_f32 v253, v90, v91 op_sel:[0,0,1]
	v_mov_b32_e32 v235, v239
	v_cvt_pk_fp8_f32 v254, v94, v95 op_sel:[0,0,1]
	v_cvt_pk_fp8_f32 v255, v98, v99 op_sel:[0,0,1]
	v_permlane32_swap_b32_e32 v239, v235
	v_add_f32_e32 v239, v239, v235
	v_fma_f32 v2, v2, v217, v239
	s_nop 1
	s_waitcnt lgkmcnt(4)
	v_mfma_f32_32x32x64_f8f6f4 v[52:67], v[248:255], v[166:173], v[52:67]
	v_mfma_f32_32x32x64_f8f6f4 v[36:51], v[248:255], v[174:181], v[36:51]
	s_waitcnt lgkmcnt(0)
	v_mfma_f32_32x32x64_f8f6f4 v[20:35], v[248:255], v[182:189], v[20:35]
	v_mfma_f32_32x32x64_f8f6f4 v[4:19], v[248:255], v[218:225], v[4:19]

.Lm_bi24:
	s_barrier
	s_add_i32 s77, s77, 1
	v_subrev_u32_e32 v215, 64, v215
	v_lshl_add_u64 v[194:195], v[194:195], 0, s[88:89]
	v_lshl_add_u64 v[196:197], v[196:197], 0, s[68:69]
	v_lshl_add_u64 v[198:199], v[198:199], 0, s[68:69]
	s_cmp_ge_u32 s77, s72
	s_cbranch_scc1 .Lm_Edrain

.Lm_nm27:
	ds_read_b128 v[166:169], v200 offset:32768
	ds_read_b128 v[174:177], v200 offset:36864
	ds_read_b128 v[170:173], v201 offset:32768
	ds_read_b128 v[178:181], v201 offset:36864
	ds_read_b128 v[182:185], v202 offset:32768
	ds_read_b128 v[218:221], v202 offset:36864
	ds_read_b128 v[186:189], v203 offset:32768
	ds_read_b128 v[222:225], v203 offset:36864
	v_max3_f32 v239, v124, v125, v126
	v_max3_f32 v235, v140, v141, v142
	v_max3_f32 v239, v239, v127, v128
	v_max3_f32 v235, v235, v143, v144
	v_max3_f32 v239, v239, v129, v130
	v_max3_f32 v235, v235, v145, v146
	v_max3_f32 v239, v239, v131, v132
	v_max3_f32 v235, v235, v147, v148
	v_max3_f32 v239, v239, v133, v134
	v_max3_f32 v235, v235, v149, v150
	v_max3_f32 v239, v239, v135, v136
	v_max3_f32 v235, v235, v151, v152
	v_max3_f32 v239, v239, v137, v138
	v_max3_f32 v235, v235, v153, v154
	v_max3_f32 v239, v239, v139, v155
	v_max_f32_e32 v239, v239, v235
	v_mov_b32_e32 v234, v239
	s_waitcnt lgkmcnt(4)
	v_mfma_f32_32x32x64_f8f6f4 v[68:83], v[166:173], v[100:107], 0
	s_nop 1
	v_permlane32_swap_b32_e32 v239, v234
	v_max_f32_e32 v239, v239, v234
	v_sub_f32_e32 v235, v239, v216
	v_mul_f32_e32 v235, 0x3a93cd3a, v235
	v_cmp_ge_f32_e32 vcc, 2.0, v235
	v_max_f32_e32 v235, v216, v239
	v_sub_f32_e32 v217, v216, v235
	v_mul_f32_e32 v217, 0x3ad53b94, v217
	v_exp_f32_e32 v217, v217
	s_cmp_eq_u64 vcc, exec
	s_cselect_b64 s[4:5], -1, 0
	v_cndmask_b32_e64 v217, v217, 1.0, s[4:5]
	v_cndmask_b32_e64 v216, v235, v216, s[4:5]
	v_cmp_gt_f32_e32 vcc, 1.0, v217
	s_cbranch_vccz .Lm_nr28
	s_and_saveexec_b64 s[6:7], s[0:1]
	ds_write_b32 v214, v217 offset:128
	s_or_b64 exec, exec, s[6:7]
	s_waitcnt lgkmcnt(0)
	ds_read_b128 v[248:251], v213 offset:128
	s_waitcnt lgkmcnt(0)
	v_pk_mul_f32 v[52:53], v[52:53], v[248:249]
	v_pk_mul_f32 v[54:55], v[54:55], v[250:251]
	v_pk_mul_f32 v[36:37], v[36:37], v[248:249]
	v_pk_mul_f32 v[38:39], v[38:39], v[250:251]
	v_pk_mul_f32 v[20:21], v[20:21], v[248:249]
	v_pk_mul_f32 v[22:23], v[22:23], v[250:251]
	v_pk_mul_f32 v[4:5], v[4:5], v[248:249]
	v_pk_mul_f32 v[6:7], v[6:7], v[250:251]
	ds_read_b128 v[248:251], v213 offset:160
	s_waitcnt lgkmcnt(0)
	v_pk_mul_f32 v[56:57], v[56:57], v[248:249]
	v_pk_mul_f32 v[58:59], v[58:59], v[250:251]
	v_pk_mul_f32 v[40:41], v[40:41], v[248:249]
	v_pk_mul_f32 v[42:43], v[42:43], v[250:251]
	v_pk_mul_f32 v[24:25], v[24:25], v[248:249]
	v_pk_mul_f32 v[26:27], v[26:27], v[250:251]
	v_pk_mul_f32 v[8:9], v[8:9], v[248:249]
	v_pk_mul_f32 v[10:11], v[10:11], v[250:251]
	ds_read_b128 v[248:251], v213 offset:192
	s_waitcnt lgkmcnt(0)
	v_pk_mul_f32 v[60:61], v[60:61], v[248:249]
	v_pk_mul_f32 v[62:63], v[62:63], v[250:251]
	v_pk_mul_f32 v[44:45], v[44:45], v[248:249]
	v_pk_mul_f32 v[46:47], v[46:47], v[250:251]
	v_pk_mul_f32 v[28:29], v[28:29], v[248:249]
	v_pk_mul_f32 v[30:31], v[30:31], v[250:251]
	v_pk_mul_f32 v[12:13], v[12:13], v[248:249]
	v_pk_mul_f32 v[14:15], v[14:15], v[250:251]
	ds_read_b128 v[248:251], v213 offset:224
	s_waitcnt lgkmcnt(0)
	v_pk_mul_f32 v[64:65], v[64:65], v[248:249]
	v_pk_mul_f32 v[66:67], v[66:67], v[250:251]
	v_pk_mul_f32 v[48:49], v[48:49], v[248:249]
	v_pk_mul_f32 v[50:51], v[50:51], v[250:251]
	v_pk_mul_f32 v[32:33], v[32:33], v[248:249]
	v_pk_mul_f32 v[34:35], v[34:35], v[250:251]
	v_pk_mul_f32 v[16:17], v[16:17], v[248:249]
	v_pk_mul_f32 v[18:19], v[18:19], v[250:251]
.Lm_nr28:
	v_fmamk_f32 v190, v216, 0xbad53b94, v210
	v_mfma_f32_32x32x64_f8f6f4 v[84:99], v[174:181], v[100:107], 0
	ds_read_b128 v[166:169], v242 offset:0
	ds_read_b128 v[174:177], v242 offset:4096
	ds_read_b128 v[170:173], v243 offset:0
	ds_read_b128 v[178:181], v243 offset:4096
	v_pk_fma_f32 v[124:125], v[124:125], s[96:97], v[190:191] op_sel_hi:[1,0,0]
	v_pk_fma_f32 v[140:141], v[140:141], s[96:97], v[190:191] op_sel_hi:[1,0,0]
	v_pk_fma_f32 v[126:127], v[126:127], s[96:97], v[190:191] op_sel_hi:[1,0,0]
	v_pk_fma_f32 v[142:143], v[142:143], s[96:97], v[190:191] op_sel_hi:[1,0,0]
	v_pk_fma_f32 v[128:129], v[128:129], s[96:97], v[190:191] op_sel_hi:[1,0,0]
	v_pk_fma_f32 v[144:145], v[144:145], s[96:97], v[190:191] op_sel_hi:[1,0,0]
	v_pk_fma_f32 v[130:131], v[130:131], s[96:97], v[190:191] op_sel_hi:[1,0,0]
	v_pk_fma_f32 v[146:147], v[146:147], s[96:97], v[190:191] op_sel_hi:[1,0,0]
	s_waitcnt lgkmcnt(4)
	v_mfma_f32_32x32x64_f8f6f4 v[68:83], v[182:189], v[108:115], v[68:83]
	v_pk_fma_f32 v[132:133], v[132:133], s[96:97], v[190:191] op_sel_hi:[1,0,0]
	v_pk_fma_f32 v[148:149], v[148:149], s[96:97], v[190:191] op_sel_hi:[1,0,0]
	v_pk_fma_f32 v[134:135], v[134:135], s[96:97], v[190:191] op_sel_hi:[1,0,0]
	v_pk_fma_f32 v[150:151], v[150:151], s[96:97], v[190:191] op_sel_hi:[1,0,0]
	v_pk_fma_f32 v[136:137], v[136:137], s[96:97], v[190:191] op_sel_hi:[1,0,0]
	v_pk_fma_f32 v[152:153], v[152:153], s[96:97], v[190:191] op_sel_hi:[1,0,0]
	v_pk_fma_f32 v[138:139], v[138:139], s[96:97], v[190:191] op_sel_hi:[1,0,0]
	v_pk_fma_f32 v[154:155], v[154:155], s[96:97], v[190:191] op_sel_hi:[1,0,0]
	v_mfma_f32_32x32x64_f8f6f4 v[84:99], v[218:225], v[108:115], v[84:99]
	v_exp_f32_e32 v124, v124
	v_exp_f32_e32 v125, v125
	v_exp_f32_e32 v126, v126
	v_exp_f32_e32 v127, v127
	v_exp_f32_e32 v128, v128
	v_exp_f32_e32 v129, v129
	v_exp_f32_e32 v130, v130
	v_exp_f32_e32 v131, v131
	s_waitcnt lgkmcnt(0)
	v_mfma_f32_32x32x64_f8f6f4 v[68:83], v[166:173], v[116:123], v[68:83]
	v_exp_f32_e32 v132, v132
	v_exp_f32_e32 v133, v133
	v_exp_f32_e32 v134, v134
	v_exp_f32_e32 v135, v135
	v_exp_f32_e32 v136, v136
	v_exp_f32_e32 v137, v137
	v_exp_f32_e32 v138, v138
	v_exp_f32_e32 v139, v139
	v_mfma_f32_32x32x64_f8f6f4 v[84:99], v[174:181], v[116:123], v[84:99]
.Lm_a26_end:
	s_sub_i32 s5, s77, 1
	s_cmp_ge_u32 s5, s42
	s_cbranch_scc1 .Lm_b29_end
	ds_read_b128 v[166:169], v207 offset:24576
	ds_read_b128 v[170:173], v208 offset:24576
	ds_read_b128 v[174:177], v207 offset:26624
	ds_read_b128 v[178:181], v208 offset:26624
	ds_read_b128 v[182:185], v207 offset:28672
	ds_read_b128 v[186:189], v208 offset:28672
	ds_read_b128 v[218:221], v207 offset:30720
	ds_read_b128 v[222:225], v208 offset:30720
	v_exp_f32_e32 v140, v140
	v_exp_f32_e32 v141, v141
	v_exp_f32_e32 v142, v142
	v_exp_f32_e32 v143, v143
	v_exp_f32_e32 v144, v144
	v_exp_f32_e32 v145, v145
	v_exp_f32_e32 v146, v146
	v_exp_f32_e32 v147, v147
	v_exp_f32_e32 v148, v148
	v_exp_f32_e32 v149, v149
	v_exp_f32_e32 v150, v150
	v_exp_f32_e32 v151, v151
	v_exp_f32_e32 v152, v152
	v_exp_f32_e32 v153, v153
	v_exp_f32_e32 v154, v154
	v_exp_f32_e32 v155, v155
	v_pk_add_f32 v[192:193], v[124:125], v[126:127]
	v_pk_add_f32 v[234:235], v[140:141], v[142:143]
	v_pk_add_f32 v[192:193], v[128:129], v[192:193]
	v_cvt_pk_fp8_f32 v248, v124, v125
	v_pk_add_f32 v[234:235], v[144:145], v[234:235]
	v_cvt_pk_fp8_f32 v249, v128, v129
	v_pk_add_f32 v[192:193], v[130:131], v[192:193]
	v_cvt_pk_fp8_f32 v250, v132, v133
	v_pk_add_f32 v[234:235], v[146:147], v[234:235]
	v_cvt_pk_fp8_f32 v251, v136, v137
	v_pk_add_f32 v[192:193], v[132:133], v[192:193]
	v_cvt_pk_fp8_f32 v252, v140, v141
	v_pk_add_f32 v[234:235], v[148:149], v[234:235]
	v_cvt_pk_fp8_f32 v253, v144, v145
	v_pk_add_f32 v[192:193], v[134:135], v[192:193]
	v_cvt_pk_fp8_f32 v254, v148, v149
	v_pk_add_f32 v[234:235], v[150:151], v[234:235]
	v_cvt_pk_fp8_f32 v255, v152, v153
	v_pk_add_f32 v[192:193], v[136:137], v[192:193]
	v_pk_add_f32 v[234:235], v[152:153], v[234:235]
	v_pk_add_f32 v[192:193], v[138:139], v[192:193]
	v_pk_add_f32 v[234:235], v[154:155], v[234:235]
	v_pk_add_f32 v[192:193], v[192:193], v[234:235]
	v_cvt_pk_fp8_f32 v248, v126, v127 op_sel:[0,0,1]
	v_cvt_pk_fp8_f32 v249, v130, v131 op_sel:[0,0,1]
	v_cvt_pk_fp8_f32 v250, v134, v135 op_sel:[0,0,1]
	v_cvt_pk_fp8_f32 v251, v138, v139 op_sel:[0,0,1]
	v_add_f32_e32 v239, v192, v193
	v_cvt_pk_fp8_f32 v252, v142, v143 op_sel:[0,0,1]
	v_cvt_pk_fp8_f32 v253, v146, v147 op_sel:[0,0,1]
	v_mov_b32_e32 v235, v239
	v_cvt_pk_fp8_f32 v254, v150, v151 op_sel:[0,0,1]
	v_cvt_pk_fp8_f32 v255, v154, v155 op_sel:[0,0,1]
	v_permlane32_swap_b32_e32 v239, v235
	v_add_f32_e32 v239, v239, v235
	v_fma_f32 v2, v2, v217, v239
	s_nop 1
	s_waitcnt lgkmcnt(4)
	v_mfma_f32_32x32x64_f8f6f4 v[52:67], v[248:255], v[166:173], v[52:67]
	v_mfma_f32_32x32x64_f8f6f4 v[36:51], v[248:255], v[174:181], v[36:51]
	s_waitcnt lgkmcnt(0)
	v_mfma_f32_32x32x64_f8f6f4 v[20:35], v[248:255], v[182:189], v[20:35]
	v_mfma_f32_32x32x64_f8f6f4 v[4:19], v[248:255], v[218:225], v[4:19]

.Lm_bs30:
	s_barrier
	s_add_i32 s77, s77, 1
	v_subrev_u32_e32 v215, 64, v215
	v_lshl_add_u64 v[194:195], v[194:195], 0, s[88:89]
	v_lshl_add_u64 v[196:197], v[196:197], 0, s[68:69]
	v_lshl_add_u64 v[198:199], v[198:199], 0, s[68:69]
	s_branch .Lm_E1

.Lm_b36_end:
	s_waitcnt vmcnt(0)
	s_cmp_eq_u32 s48, 0
	s_cbranch_scc1 .Lm_bf37
	v_pk_mul_f32 v[226:227], v[226:227], s[50:51]
	v_pk_mul_f32 v[228:229], v[228:229], s[50:51]
	v_pk_mul_f32 v[230:231], v[230:231], s[50:51]
	v_pk_mul_f32 v[232:233], v[232:233], s[50:51]
	v_med3_f32 v226, v226, s33, v212
	v_med3_f32 v227, v227, s33, v212
	v_med3_f32 v228, v228, s33, v212
	v_med3_f32 v229, v229, s33, v212
	v_med3_f32 v230, v230, s33, v212
	v_med3_f32 v231, v231, s33, v212
	v_med3_f32 v232, v232, s33, v212
	v_med3_f32 v233, v233, s33, v212
	v_cvt_pk_fp8_f32 v246, v226, v227
	v_cvt_pk_fp8_f32 v247, v230, v231
	v_cvt_pk_fp8_f32 v246, v228, v229 op_sel:[0,0,1]
	v_cvt_pk_fp8_f32 v247, v232, v233 op_sel:[0,0,1]
	global_store_dwordx4 v240, v[244:247], s[44:45]
	s_mov_b32 s48, 0

.Lm_Lstart:
	s_setprio 1
	s_add_i32 s4, s77, 1
	s_cmp_ge_u32 s4, s72
	s_cbranch_scc1 .Lm_nd38
	s_add_i32 m0, s74, 0x4000
	s_add_i32 s8, s75, 0x2000
	global_load_lds_dwordx4 v[194:195], off
	s_mov_b32 m0, s8
	s_add_i32 s8, s73, 0x4000
	global_load_lds_dwordx4 v[196:197], off
	s_mov_b32 m0, s8
	s_nop 0
	global_load_lds_dwordx4 v[198:199], off

.Lm_nd42:
	s_sub_i32 s5, s77, 2
	s_cmp_ge_u32 s5, s42
	s_cbranch_scc1 .Lm_b43_end
	ds_read_b128 v[166:169], v207 offset:24576
	ds_read_b128 v[170:173], v208 offset:24576
	ds_read_b128 v[174:177], v207 offset:26624
	ds_read_b128 v[178:181], v208 offset:26624
	ds_read_b128 v[182:185], v207 offset:28672
	ds_read_b128 v[186:189], v208 offset:28672
	ds_read_b128 v[218:221], v207 offset:30720
	ds_read_b128 v[222:225], v208 offset:30720
	v_exp_f32_e32 v140, v140
	v_exp_f32_e32 v141, v141
	v_exp_f32_e32 v142, v142
	v_exp_f32_e32 v143, v143
	v_exp_f32_e32 v144, v144
	v_exp_f32_e32 v145, v145
	v_exp_f32_e32 v146, v146
	v_exp_f32_e32 v147, v147
	v_exp_f32_e32 v148, v148
	v_exp_f32_e32 v149, v149
	v_exp_f32_e32 v150, v150
	v_exp_f32_e32 v151, v151
	v_exp_f32_e32 v152, v152
	v_exp_f32_e32 v153, v153
	v_exp_f32_e32 v154, v154
	v_exp_f32_e32 v155, v155
	v_pk_add_f32 v[192:193], v[124:125], v[126:127]
	v_pk_add_f32 v[234:235], v[140:141], v[142:143]
	v_pk_add_f32 v[192:193], v[128:129], v[192:193]
	v_cvt_pk_fp8_f32 v248, v124, v125
	v_pk_add_f32 v[234:235], v[144:145], v[234:235]
	v_cvt_pk_fp8_f32 v249, v128, v129
	v_pk_add_f32 v[192:193], v[130:131], v[192:193]
	v_cvt_pk_fp8_f32 v250, v132, v133
	v_pk_add_f32 v[234:235], v[146:147], v[234:235]
	v_cvt_pk_fp8_f32 v251, v136, v137
	v_pk_add_f32 v[192:193], v[132:133], v[192:193]
	v_cvt_pk_fp8_f32 v252, v140, v141
	v_pk_add_f32 v[234:235], v[148:149], v[234:235]
	v_cvt_pk_fp8_f32 v253, v144, v145
	v_pk_add_f32 v[192:193], v[134:135], v[192:193]
	v_cvt_pk_fp8_f32 v254, v148, v149
	v_pk_add_f32 v[234:235], v[150:151], v[234:235]
	v_cvt_pk_fp8_f32 v255, v152, v153
	v_pk_add_f32 v[192:193], v[136:137], v[192:193]
	v_pk_add_f32 v[234:235], v[152:153], v[234:235]
	v_pk_add_f32 v[192:193], v[138:139], v[192:193]
	v_pk_add_f32 v[234:235], v[154:155], v[234:235]
	v_pk_add_f32 v[192:193], v[192:193], v[234:235]
	v_cvt_pk_fp8_f32 v248, v126, v127 op_sel:[0,0,1]
	v_cvt_pk_fp8_f32 v249, v130, v131 op_sel:[0,0,1]
	v_cvt_pk_fp8_f32 v250, v134, v135 op_sel:[0,0,1]
	v_cvt_pk_fp8_f32 v251, v138, v139 op_sel:[0,0,1]
	v_add_f32_e32 v239, v192, v193
	v_cvt_pk_fp8_f32 v252, v142, v143 op_sel:[0,0,1]
	v_cvt_pk_fp8_f32 v253, v146, v147 op_sel:[0,0,1]
	v_mov_b32_e32 v235, v239
	v_cvt_pk_fp8_f32 v254, v150, v151 op_sel:[0,0,1]
	v_cvt_pk_fp8_f32 v255, v154, v155 op_sel:[0,0,1]
	v_permlane32_swap_b32_e32 v239, v235
	v_add_f32_e32 v239, v239, v235
	v_fma_f32 v2, v2, v217, v239
	s_nop 1
	s_waitcnt lgkmcnt(4)
	v_mfma_f32_32x32x64_f8f6f4 v[52:67], v[248:255], v[166:173], v[52:67]
	v_mfma_f32_32x32x64_f8f6f4 v[36:51], v[248:255], v[174:181], v[36:51]
	s_waitcnt lgkmcnt(0)
	v_mfma_f32_32x32x64_f8f6f4 v[20:35], v[248:255], v[182:189], v[20:35]
	v_mfma_f32_32x32x64_f8f6f4 v[4:19], v[248:255], v[218:225], v[4:19]

.Lm_nd48:
	s_sub_i32 s5, s77, 2
	s_cmp_ge_u32 s5, s42
	s_cbranch_scc1 .Lm_b49_end
	ds_read_b128 v[166:169], v207 offset:0
	ds_read_b128 v[170:173], v208 offset:0
	ds_read_b128 v[174:177], v207 offset:2048
	ds_read_b128 v[178:181], v208 offset:2048
	ds_read_b128 v[182:185], v207 offset:4096
	ds_read_b128 v[186:189], v208 offset:4096
	ds_read_b128 v[218:221], v207 offset:6144
	ds_read_b128 v[222:225], v208 offset:6144
	v_exp_f32_e32 v84, v84
	v_exp_f32_e32 v85, v85
	v_exp_f32_e32 v86, v86
	v_exp_f32_e32 v87, v87
	v_exp_f32_e32 v88, v88
	v_exp_f32_e32 v89, v89
	v_exp_f32_e32 v90, v90
	v_exp_f32_e32 v91, v91
	v_exp_f32_e32 v92, v92
	v_exp_f32_e32 v93, v93
	v_exp_f32_e32 v94, v94
	v_exp_f32_e32 v95, v95
	v_exp_f32_e32 v96, v96
	v_exp_f32_e32 v97, v97
	v_exp_f32_e32 v98, v98
	v_exp_f32_e32 v99, v99
	v_pk_add_f32 v[192:193], v[68:69], v[70:71]
	v_pk_add_f32 v[234:235], v[84:85], v[86:87]
	v_pk_add_f32 v[192:193], v[72:73], v[192:193]
	v_cvt_pk_fp8_f32 v248, v68, v69
	v_pk_add_f32 v[234:235], v[88:89], v[234:235]
	v_cvt_pk_fp8_f32 v249, v72, v73
	v_pk_add_f32 v[192:193], v[74:75], v[192:193]
	v_cvt_pk_fp8_f32 v250, v76, v77
	v_pk_add_f32 v[234:235], v[90:91], v[234:235]
	v_cvt_pk_fp8_f32 v251, v80, v81
	v_pk_add_f32 v[192:193], v[76:77], v[192:193]
	v_cvt_pk_fp8_f32 v252, v84, v85
	v_pk_add_f32 v[234:235], v[92:93], v[234:235]
	v_cvt_pk_fp8_f32 v253, v88, v89
	v_pk_add_f32 v[192:193], v[78:79], v[192:193]
	v_cvt_pk_fp8_f32 v254, v92, v93
	v_pk_add_f32 v[234:235], v[94:95], v[234:235]
	v_cvt_pk_fp8_f32 v255, v96, v97
	v_pk_add_f32 v[192:193], v[80:81], v[192:193]
	v_pk_add_f32 v[234:235], v[96:97], v[234:235]
	v_pk_add_f32 v[192:193], v[82:83], v[192:193]
	v_pk_add_f32 v[234:235], v[98:99], v[234:235]
	v_pk_add_f32 v[192:193], v[192:193], v[234:235]
	v_cvt_pk_fp8_f32 v248, v70, v71 op_sel:[0,0,1]
	v_cvt_pk_fp8_f32 v249, v74, v75 op_sel:[0,0,1]
	v_cvt_pk_fp8_f32 v250, v78, v79 op_sel:[0,0,1]
	v_cvt_pk_fp8_f32 v251, v82, v83 op_sel:[0,0,1]
	v_add_f32_e32 v239, v192, v193
	v_cvt_pk_fp8_f32 v252, v86, v87 op_sel:[0,0,1]
	v_cvt_pk_fp8_f32 v253, v90, v91 op_sel:[0,0,1]
	v_mov_b32_e32 v235, v239
	v_cvt_pk_fp8_f32 v254, v94, v95 op_sel:[0,0,1]
	v_cvt_pk_fp8_f32 v255, v98, v99 op_sel:[0,0,1]
	v_permlane32_swap_b32_e32 v239, v235
	v_add_f32_e32 v239, v239, v235
	v_fma_f32 v2, v2, v217, v239
	s_nop 1
	s_waitcnt lgkmcnt(4)
	v_mfma_f32_32x32x64_f8f6f4 v[52:67], v[248:255], v[166:173], v[52:67]
	v_mfma_f32_32x32x64_f8f6f4 v[36:51], v[248:255], v[174:181], v[36:51]
	s_waitcnt lgkmcnt(0)
	v_mfma_f32_32x32x64_f8f6f4 v[20:35], v[248:255], v[182:189], v[20:35]
	v_mfma_f32_32x32x64_f8f6f4 v[4:19], v[248:255], v[218:225], v[4:19]

.Lm_nd56:
	s_sub_i32 s5, s77, 2
	s_cmp_ge_u32 s5, s42
	s_cbranch_scc1 .Lm_b57_end
	ds_read_b128 v[166:169], v207 offset:16384
	ds_read_b128 v[170:173], v208 offset:16384
	ds_read_b128 v[174:177], v207 offset:18432
	ds_read_b128 v[178:181], v208 offset:18432
	ds_read_b128 v[182:185], v207 offset:20480
	ds_read_b128 v[186:189], v208 offset:20480
	ds_read_b128 v[218:221], v207 offset:22528
	ds_read_b128 v[222:225], v208 offset:22528
	v_exp_f32_e32 v140, v140
	v_exp_f32_e32 v141, v141
	v_exp_f32_e32 v142, v142
	v_exp_f32_e32 v143, v143
	v_exp_f32_e32 v144, v144
	v_exp_f32_e32 v145, v145
	v_exp_f32_e32 v146, v146
	v_exp_f32_e32 v147, v147
	v_exp_f32_e32 v148, v148
	v_exp_f32_e32 v149, v149
	v_exp_f32_e32 v150, v150
	v_exp_f32_e32 v151, v151
	v_exp_f32_e32 v152, v152
	v_exp_f32_e32 v153, v153
	v_exp_f32_e32 v154, v154
	v_exp_f32_e32 v155, v155
	v_pk_add_f32 v[192:193], v[124:125], v[126:127]
	v_pk_add_f32 v[234:235], v[140:141], v[142:143]
	v_pk_add_f32 v[192:193], v[128:129], v[192:193]
	v_cvt_pk_fp8_f32 v248, v124, v125
	v_pk_add_f32 v[234:235], v[144:145], v[234:235]
	v_cvt_pk_fp8_f32 v249, v128, v129
	v_pk_add_f32 v[192:193], v[130:131], v[192:193]
	v_cvt_pk_fp8_f32 v250, v132, v133
	v_pk_add_f32 v[234:235], v[146:147], v[234:235]
	v_cvt_pk_fp8_f32 v251, v136, v137
	v_pk_add_f32 v[192:193], v[132:133], v[192:193]
	v_cvt_pk_fp8_f32 v252, v140, v141
	v_pk_add_f32 v[234:235], v[148:149], v[234:235]
	v_cvt_pk_fp8_f32 v253, v144, v145
	v_pk_add_f32 v[192:193], v[134:135], v[192:193]
	v_cvt_pk_fp8_f32 v254, v148, v149
	v_pk_add_f32 v[234:235], v[150:151], v[234:235]
	v_cvt_pk_fp8_f32 v255, v152, v153
	v_pk_add_f32 v[192:193], v[136:137], v[192:193]
	v_pk_add_f32 v[234:235], v[152:153], v[234:235]
	v_pk_add_f32 v[192:193], v[138:139], v[192:193]
	v_pk_add_f32 v[234:235], v[154:155], v[234:235]
	v_pk_add_f32 v[192:193], v[192:193], v[234:235]
	v_cvt_pk_fp8_f32 v248, v126, v127 op_sel:[0,0,1]
	v_cvt_pk_fp8_f32 v249, v130, v131 op_sel:[0,0,1]
	v_cvt_pk_fp8_f32 v250, v134, v135 op_sel:[0,0,1]
	v_cvt_pk_fp8_f32 v251, v138, v139 op_sel:[0,0,1]
	v_add_f32_e32 v239, v192, v193
	v_cvt_pk_fp8_f32 v252, v142, v143 op_sel:[0,0,1]
	v_cvt_pk_fp8_f32 v253, v146, v147 op_sel:[0,0,1]
	v_mov_b32_e32 v235, v239
	v_cvt_pk_fp8_f32 v254, v150, v151 op_sel:[0,0,1]
	v_cvt_pk_fp8_f32 v255, v154, v155 op_sel:[0,0,1]
	v_permlane32_swap_b32_e32 v239, v235
	v_add_f32_e32 v239, v239, v235
	v_fma_f32 v2, v2, v217, v239
	s_nop 1
	s_waitcnt lgkmcnt(4)
	v_mfma_f32_32x32x64_f8f6f4 v[52:67], v[248:255], v[166:173], v[52:67]
	v_mfma_f32_32x32x64_f8f6f4 v[36:51], v[248:255], v[174:181], v[36:51]
	s_waitcnt lgkmcnt(0)
	v_mfma_f32_32x32x64_f8f6f4 v[20:35], v[248:255], v[182:189], v[20:35]
	v_mfma_f32_32x32x64_f8f6f4 v[4:19], v[248:255], v[218:225], v[4:19]

.Lm_nd62:
	s_sub_i32 s5, s77, 2
	s_cmp_ge_u32 s5, s42
	s_cbranch_scc1 .Lm_b63_end
	ds_read_b128 v[166:169], v207 offset:8192
	ds_read_b128 v[170:173], v208 offset:8192
	ds_read_b128 v[174:177], v207 offset:10240
	ds_read_b128 v[178:181], v208 offset:10240
	ds_read_b128 v[182:185], v207 offset:12288
	ds_read_b128 v[186:189], v208 offset:12288
	ds_read_b128 v[218:221], v207 offset:14336
	ds_read_b128 v[222:225], v208 offset:14336
	v_exp_f32_e32 v84, v84
	v_exp_f32_e32 v85, v85
	v_exp_f32_e32 v86, v86
	v_exp_f32_e32 v87, v87
	v_exp_f32_e32 v88, v88
	v_exp_f32_e32 v89, v89
	v_exp_f32_e32 v90, v90
	v_exp_f32_e32 v91, v91
	v_exp_f32_e32 v92, v92
	v_exp_f32_e32 v93, v93
	v_exp_f32_e32 v94, v94
	v_exp_f32_e32 v95, v95
	v_exp_f32_e32 v96, v96
	v_exp_f32_e32 v97, v97
	v_exp_f32_e32 v98, v98
	v_exp_f32_e32 v99, v99
	v_pk_add_f32 v[192:193], v[68:69], v[70:71]
	v_pk_add_f32 v[234:235], v[84:85], v[86:87]
	v_pk_add_f32 v[192:193], v[72:73], v[192:193]
	v_cvt_pk_fp8_f32 v248, v68, v69
	v_pk_add_f32 v[234:235], v[88:89], v[234:235]
	v_cvt_pk_fp8_f32 v249, v72, v73
	v_pk_add_f32 v[192:193], v[74:75], v[192:193]
	v_cvt_pk_fp8_f32 v250, v76, v77
	v_pk_add_f32 v[234:235], v[90:91], v[234:235]
	v_cvt_pk_fp8_f32 v251, v80, v81
	v_pk_add_f32 v[192:193], v[76:77], v[192:193]
	v_cvt_pk_fp8_f32 v252, v84, v85
	v_pk_add_f32 v[234:235], v[92:93], v[234:235]
	v_cvt_pk_fp8_f32 v253, v88, v89
	v_pk_add_f32 v[192:193], v[78:79], v[192:193]
	v_cvt_pk_fp8_f32 v254, v92, v93
	v_pk_add_f32 v[234:235], v[94:95], v[234:235]
	v_cvt_pk_fp8_f32 v255, v96, v97
	v_pk_add_f32 v[192:193], v[80:81], v[192:193]
	v_pk_add_f32 v[234:235], v[96:97], v[234:235]
	v_pk_add_f32 v[192:193], v[82:83], v[192:193]
	v_pk_add_f32 v[234:235], v[98:99], v[234:235]
	v_pk_add_f32 v[192:193], v[192:193], v[234:235]
	v_cvt_pk_fp8_f32 v248, v70, v71 op_sel:[0,0,1]
	v_cvt_pk_fp8_f32 v249, v74, v75 op_sel:[0,0,1]
	v_cvt_pk_fp8_f32 v250, v78, v79 op_sel:[0,0,1]
	v_cvt_pk_fp8_f32 v251, v82, v83 op_sel:[0,0,1]
	v_add_f32_e32 v239, v192, v193
	v_cvt_pk_fp8_f32 v252, v86, v87 op_sel:[0,0,1]
	v_cvt_pk_fp8_f32 v253, v90, v91 op_sel:[0,0,1]
	v_mov_b32_e32 v235, v239
	v_cvt_pk_fp8_f32 v254, v94, v95 op_sel:[0,0,1]
	v_cvt_pk_fp8_f32 v255, v98, v99 op_sel:[0,0,1]
	v_permlane32_swap_b32_e32 v239, v235
	v_add_f32_e32 v239, v239, v235
	v_fma_f32 v2, v2, v217, v239
	s_nop 1
	s_waitcnt lgkmcnt(4)
	v_mfma_f32_32x32x64_f8f6f4 v[52:67], v[248:255], v[166:173], v[52:67]
	v_mfma_f32_32x32x64_f8f6f4 v[36:51], v[248:255], v[174:181], v[36:51]
	s_waitcnt lgkmcnt(0)
	v_mfma_f32_32x32x64_f8f6f4 v[20:35], v[248:255], v[182:189], v[20:35]
	v_mfma_f32_32x32x64_f8f6f4 v[4:19], v[248:255], v[218:225], v[4:19]

.Lm_a6_slow:
	s_cmp_lg_u32 s77, s42
	s_cbranch_scc1 .Lm_a6_end
	s_cmp_le_u32 s77, s43
	s_cbranch_scc1 .Lm_nm76
	v_add_u32_e32 v239, 64, v215
	v_cmp_gt_i32_e64 s[4:5], 0, v239
	v_cmp_gt_i32_e64 s[6:7], 1, v239
	v_cmp_gt_i32_e64 s[8:9], 2, v239
	v_cmp_gt_i32_e64 s[10:11], 3, v239
	v_cndmask_b32_e64 v68, v68, v211, s[4:5]
	v_cndmask_b32_e64 v69, v69, v211, s[6:7]
	v_cndmask_b32_e64 v70, v70, v211, s[8:9]
	v_cndmask_b32_e64 v71, v71, v211, s[10:11]
	v_cmp_gt_i32_e64 s[4:5], 8, v239
	v_cmp_gt_i32_e64 s[6:7], 9, v239
	v_cmp_gt_i32_e64 s[8:9], 10, v239
	v_cmp_gt_i32_e64 s[10:11], 11, v239
	v_cndmask_b32_e64 v72, v72, v211, s[4:5]
	v_cndmask_b32_e64 v73, v73, v211, s[6:7]
	v_cndmask_b32_e64 v74, v74, v211, s[8:9]
	v_cndmask_b32_e64 v75, v75, v211, s[10:11]
	v_cmp_gt_i32_e64 s[4:5], 16, v239
	v_cmp_gt_i32_e64 s[6:7], 17, v239
	v_cmp_gt_i32_e64 s[8:9], 18, v239
	v_cmp_gt_i32_e64 s[10:11], 19, v239
	v_cndmask_b32_e64 v76, v76, v211, s[4:5]
	v_cndmask_b32_e64 v77, v77, v211, s[6:7]
	v_cndmask_b32_e64 v78, v78, v211, s[8:9]
	v_cndmask_b32_e64 v79, v79, v211, s[10:11]
	v_cmp_gt_i32_e64 s[4:5], 24, v239
	v_cmp_gt_i32_e64 s[6:7], 25, v239
	v_cmp_gt_i32_e64 s[8:9], 26, v239
	v_cmp_gt_i32_e64 s[10:11], 27, v239
	v_cndmask_b32_e64 v80, v80, v211, s[4:5]
	v_cndmask_b32_e64 v81, v81, v211, s[6:7]
	v_cndmask_b32_e64 v82, v82, v211, s[8:9]
	v_cndmask_b32_e64 v83, v83, v211, s[10:11]
	v_cmp_gt_i32_e64 s[4:5], 32, v239
	v_cmp_gt_i32_e64 s[6:7], 33, v239
	v_cmp_gt_i32_e64 s[8:9], 34, v239
	v_cmp_gt_i32_e64 s[10:11], 35, v239
	v_cndmask_b32_e64 v84, v84, v211, s[4:5]
	v_cndmask_b32_e64 v85, v85, v211, s[6:7]
	v_cndmask_b32_e64 v86, v86, v211, s[8:9]
	v_cndmask_b32_e64 v87, v87, v211, s[10:11]
	v_cmp_gt_i32_e64 s[4:5], 40, v239
	v_cmp_gt_i32_e64 s[6:7], 41, v239
	v_cmp_gt_i32_e64 s[8:9], 42, v239
	v_cmp_gt_i32_e64 s[10:11], 43, v239
	v_cndmask_b32_e64 v88, v88, v211, s[4:5]
	v_cndmask_b32_e64 v89, v89, v211, s[6:7]
	v_cndmask_b32_e64 v90, v90, v211, s[8:9]
	v_cndmask_b32_e64 v91, v91, v211, s[10:11]
	v_cmp_gt_i32_e64 s[4:5], 48, v239
	v_cmp_gt_i32_e64 s[6:7], 49, v239
	v_cmp_gt_i32_e64 s[8:9], 50, v239
	v_cmp_gt_i32_e64 s[10:11], 51, v239
	v_cndmask_b32_e64 v92, v92, v211, s[4:5]
	v_cndmask_b32_e64 v93, v93, v211, s[6:7]
	v_cndmask_b32_e64 v94, v94, v211, s[8:9]
	v_cndmask_b32_e64 v95, v95, v211, s[10:11]
	v_cmp_gt_i32_e64 s[4:5], 56, v239
	v_cmp_gt_i32_e64 s[6:7], 57, v239
	v_cmp_gt_i32_e64 s[8:9], 58, v239
	v_cmp_gt_i32_e64 s[10:11], 59, v239
	v_cndmask_b32_e64 v96, v96, v211, s[4:5]
	v_cndmask_b32_e64 v97, v97, v211, s[6:7]
	v_cndmask_b32_e64 v98, v98, v211, s[8:9]
	v_cndmask_b32_e64 v99, v99, v211, s[10:11]

.Lm_nr77:
	v_fmamk_f32 v190, v216, 0xbad53b94, v210
	v_pk_fma_f32 v[68:69], v[68:69], s[96:97], v[190:191] op_sel_hi:[1,0,0]
	v_pk_fma_f32 v[84:85], v[84:85], s[96:97], v[190:191] op_sel_hi:[1,0,0]
	v_pk_fma_f32 v[70:71], v[70:71], s[96:97], v[190:191] op_sel_hi:[1,0,0]
	v_pk_fma_f32 v[86:87], v[86:87], s[96:97], v[190:191] op_sel_hi:[1,0,0]
	v_pk_fma_f32 v[72:73], v[72:73], s[96:97], v[190:191] op_sel_hi:[1,0,0]
	v_pk_fma_f32 v[88:89], v[88:89], s[96:97], v[190:191] op_sel_hi:[1,0,0]
	v_pk_fma_f32 v[74:75], v[74:75], s[96:97], v[190:191] op_sel_hi:[1,0,0]
	v_pk_fma_f32 v[90:91], v[90:91], s[96:97], v[190:191] op_sel_hi:[1,0,0]
	v_pk_fma_f32 v[76:77], v[76:77], s[96:97], v[190:191] op_sel_hi:[1,0,0]
	v_pk_fma_f32 v[92:93], v[92:93], s[96:97], v[190:191] op_sel_hi:[1,0,0]
	v_pk_fma_f32 v[78:79], v[78:79], s[96:97], v[190:191] op_sel_hi:[1,0,0]
	v_pk_fma_f32 v[94:95], v[94:95], s[96:97], v[190:191] op_sel_hi:[1,0,0]
	v_pk_fma_f32 v[80:81], v[80:81], s[96:97], v[190:191] op_sel_hi:[1,0,0]
	v_pk_fma_f32 v[96:97], v[96:97], s[96:97], v[190:191] op_sel_hi:[1,0,0]
	v_pk_fma_f32 v[82:83], v[82:83], s[96:97], v[190:191] op_sel_hi:[1,0,0]
	v_pk_fma_f32 v[98:99], v[98:99], s[96:97], v[190:191] op_sel_hi:[1,0,0]
	v_exp_f32_e32 v68, v68
	v_exp_f32_e32 v69, v69
	v_exp_f32_e32 v70, v70
	v_exp_f32_e32 v71, v71
	v_exp_f32_e32 v72, v72
	v_exp_f32_e32 v73, v73
	v_exp_f32_e32 v74, v74
	v_exp_f32_e32 v75, v75
	v_exp_f32_e32 v76, v76
	v_exp_f32_e32 v77, v77
	v_exp_f32_e32 v78, v78
	v_exp_f32_e32 v79, v79
	v_exp_f32_e32 v80, v80
	v_exp_f32_e32 v81, v81
	v_exp_f32_e32 v82, v82
	v_exp_f32_e32 v83, v83
	s_branch .Lm_a6_end
.Lm_a12_slow:
	s_cmp_lg_u32 s77, s42
	s_cbranch_scc1 .Lm_a12_end
	s_cmp_le_u32 s77, s43
	s_cbranch_scc1 .Lm_nm78
	v_add_u32_e32 v239, 64, v215
	v_cmp_gt_i32_e64 s[4:5], 0, v239
	v_cmp_gt_i32_e64 s[6:7], 1, v239
	v_cmp_gt_i32_e64 s[8:9], 2, v239
	v_cmp_gt_i32_e64 s[10:11], 3, v239
	v_cndmask_b32_e64 v124, v124, v211, s[4:5]
	v_cndmask_b32_e64 v125, v125, v211, s[6:7]
	v_cndmask_b32_e64 v126, v126, v211, s[8:9]
	v_cndmask_b32_e64 v127, v127, v211, s[10:11]
	v_cmp_gt_i32_e64 s[4:5], 8, v239
	v_cmp_gt_i32_e64 s[6:7], 9, v239
	v_cmp_gt_i32_e64 s[8:9], 10, v239
	v_cmp_gt_i32_e64 s[10:11], 11, v239
	v_cndmask_b32_e64 v128, v128, v211, s[4:5]
	v_cndmask_b32_e64 v129, v129, v211, s[6:7]
	v_cndmask_b32_e64 v130, v130, v211, s[8:9]
	v_cndmask_b32_e64 v131, v131, v211, s[10:11]
	v_cmp_gt_i32_e64 s[4:5], 16, v239
	v_cmp_gt_i32_e64 s[6:7], 17, v239
	v_cmp_gt_i32_e64 s[8:9], 18, v239
	v_cmp_gt_i32_e64 s[10:11], 19, v239
	v_cndmask_b32_e64 v132, v132, v211, s[4:5]
	v_cndmask_b32_e64 v133, v133, v211, s[6:7]
	v_cndmask_b32_e64 v134, v134, v211, s[8:9]
	v_cndmask_b32_e64 v135, v135, v211, s[10:11]
	v_cmp_gt_i32_e64 s[4:5], 24, v239
	v_cmp_gt_i32_e64 s[6:7], 25, v239
	v_cmp_gt_i32_e64 s[8:9], 26, v239
	v_cmp_gt_i32_e64 s[10:11], 27, v239
	v_cndmask_b32_e64 v136, v136, v211, s[4:5]
	v_cndmask_b32_e64 v137, v137, v211, s[6:7]
	v_cndmask_b32_e64 v138, v138, v211, s[8:9]
	v_cndmask_b32_e64 v139, v139, v211, s[10:11]
	v_cmp_gt_i32_e64 s[4:5], 32, v239
	v_cmp_gt_i32_e64 s[6:7], 33, v239
	v_cmp_gt_i32_e64 s[8:9], 34, v239
	v_cmp_gt_i32_e64 s[10:11], 35, v239
	v_cndmask_b32_e64 v140, v140, v211, s[4:5]
	v_cndmask_b32_e64 v141, v141, v211, s[6:7]
	v_cndmask_b32_e64 v142, v142, v211, s[8:9]
	v_cndmask_b32_e64 v143, v143, v211, s[10:11]
	v_cmp_gt_i32_e64 s[4:5], 40, v239
	v_cmp_gt_i32_e64 s[6:7], 41, v239
	v_cmp_gt_i32_e64 s[8:9], 42, v239
	v_cmp_gt_i32_e64 s[10:11], 43, v239
	v_cndmask_b32_e64 v144, v144, v211, s[4:5]
	v_cndmask_b32_e64 v145, v145, v211, s[6:7]
	v_cndmask_b32_e64 v146, v146, v211, s[8:9]
	v_cndmask_b32_e64 v147, v147, v211, s[10:11]
	v_cmp_gt_i32_e64 s[4:5], 48, v239
	v_cmp_gt_i32_e64 s[6:7], 49, v239
	v_cmp_gt_i32_e64 s[8:9], 50, v239
	v_cmp_gt_i32_e64 s[10:11], 51, v239
	v_cndmask_b32_e64 v148, v148, v211, s[4:5]
	v_cndmask_b32_e64 v149, v149, v211, s[6:7]
	v_cndmask_b32_e64 v150, v150, v211, s[8:9]
	v_cndmask_b32_e64 v151, v151, v211, s[10:11]
	v_cmp_gt_i32_e64 s[4:5], 56, v239
	v_cmp_gt_i32_e64 s[6:7], 57, v239
	v_cmp_gt_i32_e64 s[8:9], 58, v239
	v_cmp_gt_i32_e64 s[10:11], 59, v239
	v_cndmask_b32_e64 v152, v152, v211, s[4:5]
	v_cndmask_b32_e64 v153, v153, v211, s[6:7]
	v_cndmask_b32_e64 v154, v154, v211, s[8:9]
	v_cndmask_b32_e64 v155, v155, v211, s[10:11]

.Lm_nr79:
	v_fmamk_f32 v190, v216, 0xbad53b94, v210
	v_pk_fma_f32 v[124:125], v[124:125], s[96:97], v[190:191] op_sel_hi:[1,0,0]
	v_pk_fma_f32 v[140:141], v[140:141], s[96:97], v[190:191] op_sel_hi:[1,0,0]
	v_pk_fma_f32 v[126:127], v[126:127], s[96:97], v[190:191] op_sel_hi:[1,0,0]
	v_pk_fma_f32 v[142:143], v[142:143], s[96:97], v[190:191] op_sel_hi:[1,0,0]
	v_pk_fma_f32 v[128:129], v[128:129], s[96:97], v[190:191] op_sel_hi:[1,0,0]
	v_pk_fma_f32 v[144:145], v[144:145], s[96:97], v[190:191] op_sel_hi:[1,0,0]
	v_pk_fma_f32 v[130:131], v[130:131], s[96:97], v[190:191] op_sel_hi:[1,0,0]
	v_pk_fma_f32 v[146:147], v[146:147], s[96:97], v[190:191] op_sel_hi:[1,0,0]
	v_pk_fma_f32 v[132:133], v[132:133], s[96:97], v[190:191] op_sel_hi:[1,0,0]
	v_pk_fma_f32 v[148:149], v[148:149], s[96:97], v[190:191] op_sel_hi:[1,0,0]
	v_pk_fma_f32 v[134:135], v[134:135], s[96:97], v[190:191] op_sel_hi:[1,0,0]
	v_pk_fma_f32 v[150:151], v[150:151], s[96:97], v[190:191] op_sel_hi:[1,0,0]
	v_pk_fma_f32 v[136:137], v[136:137], s[96:97], v[190:191] op_sel_hi:[1,0,0]
	v_pk_fma_f32 v[152:153], v[152:153], s[96:97], v[190:191] op_sel_hi:[1,0,0]
	v_pk_fma_f32 v[138:139], v[138:139], s[96:97], v[190:191] op_sel_hi:[1,0,0]
	v_pk_fma_f32 v[154:155], v[154:155], s[96:97], v[190:191] op_sel_hi:[1,0,0]
	v_exp_f32_e32 v124, v124
	v_exp_f32_e32 v125, v125
	v_exp_f32_e32 v126, v126
	v_exp_f32_e32 v127, v127
	v_exp_f32_e32 v128, v128
	v_exp_f32_e32 v129, v129
	v_exp_f32_e32 v130, v130
	v_exp_f32_e32 v131, v131
	v_exp_f32_e32 v132, v132
	v_exp_f32_e32 v133, v133
	v_exp_f32_e32 v134, v134
	v_exp_f32_e32 v135, v135
	v_exp_f32_e32 v136, v136
	v_exp_f32_e32 v137, v137
	v_exp_f32_e32 v138, v138
	v_exp_f32_e32 v139, v139
	s_branch .Lm_a12_end

.Lm_exit:
	s_setprio 0
	s_mov_b32 m0, s40
	v_or_b32_e32 v166, 0x1000, v164
	v_mov_b32_e32 v167, v3
	v_or_b32_e32 v168, 0x1800, v164
	v_mov_b32_e32 v169, v3
	v_or_b32_e32 v170, 0x4000, v164
	v_mov_b32_e32 v171, v3
	v_or_b32_e32 v172, 0x4800, v164
	v_mov_b32_e32 v173, v3
	v_or_b32_e32 v174, 0x5000, v164
	v_mov_b32_e32 v175, v3
	v_or_b32_e32 v176, 0x5800, v164
	v_mov_b32_e32 v177, v3
	v_or_b32_e32 v178, 0x8000, v164
	v_mov_b32_e32 v179, v3
	v_or_b32_e32 v180, 0x8800, v164
	v_mov_b32_e32 v181, v3
	v_or_b32_e32 v182, 0x9000, v164
	v_mov_b32_e32 v183, v3
	v_or_b32_e32 v184, 0x9800, v164
	v_mov_b32_e32 v185, v3
	v_or_b32_e32 v186, 0xc000, v164
	v_mov_b32_e32 v187, v3
	v_or_b32_e32 v188, 0xc800, v164
	v_mov_b32_e32 v189, v3
	v_or_b32_e32 v190, 0xd000, v164
	v_mov_b32_e32 v191, v3
	v_or_b32_e32 v192, 0xd800, v164
	v_mov_b32_e32 v193, v3
	s_branch .LBB0_1022

	.amdhsa_kernel _Z10hybrid_fwd6Params
		.amdhsa_group_segment_fixed_size 0
		.amdhsa_private_segment_fixed_size 0
		.amdhsa_kernarg_size 1080
		.amdhsa_user_sgpr_count 2
		.amdhsa_user_sgpr_dispatch_ptr 0
		.amdhsa_user_sgpr_queue_ptr 0
		.amdhsa_user_sgpr_kernarg_segment_ptr 1
		.amdhsa_user_sgpr_dispatch_id 0
		.amdhsa_user_sgpr_kernarg_preload_length 0
		.amdhsa_user_sgpr_kernarg_preload_offset 0
		.amdhsa_user_sgpr_private_segment_size 0
		.amdhsa_uses_dynamic_stack 0
		.amdhsa_enable_private_segment 0
		.amdhsa_system_sgpr_workgroup_id_x 1
		.amdhsa_system_sgpr_workgroup_id_y 0
		.amdhsa_system_sgpr_workgroup_id_z 0
		.amdhsa_system_sgpr_workgroup_info 0
		.amdhsa_system_vgpr_workitem_id 0
		.amdhsa_next_free_vgpr 256
		.amdhsa_next_free_sgpr 98
		.amdhsa_accum_offset 256
		.amdhsa_reserve_vcc 1
		.amdhsa_float_round_mode_32 0
		.amdhsa_float_round_mode_16_64 0
		.amdhsa_float_denorm_mode_32 3
		.amdhsa_float_denorm_mode_16_64 3
		.amdhsa_dx10_clamp 1
		.amdhsa_ieee_mode 1
		.amdhsa_fp16_overflow 0
		.amdhsa_tg_split 0
		.amdhsa_exception_fp_ieee_invalid_op 0
		.amdhsa_exception_fp_denorm_src 0
		.amdhsa_exception_fp_ieee_div_zero 0
		.amdhsa_exception_fp_ieee_overflow 0
		.amdhsa_exception_fp_ieee_underflow 0
		.amdhsa_exception_fp_ieee_inexact 0
		.amdhsa_exception_int_div_zero 0
	.end_amdhsa_kernel

amdhsa.kernels:
  - .agpr_count:     0
    .args:
      - .offset:         0
        .size:           824
        .value_kind:     by_value
      - .offset:         824
        .size:           4
        .value_kind:     hidden_block_count_x
      - .offset:         828
        .size:           4
        .value_kind:     hidden_block_count_y
      - .offset:         832
        .size:           4
        .value_kind:     hidden_block_count_z
      - .offset:         836
        .size:           2
        .value_kind:     hidden_group_size_x
      - .offset:         838
        .size:           2
        .value_kind:     hidden_group_size_y
      - .offset:         840
        .size:           2
        .value_kind:     hidden_group_size_z
      - .offset:         842
        .size:           2
        .value_kind:     hidden_remainder_x
      - .offset:         844
        .size:           2
        .value_kind:     hidden_remainder_y
      - .offset:         846
        .size:           2
        .value_kind:     hidden_remainder_z
      - .offset:         864
        .size:           8
        .value_kind:     hidden_global_offset_x
      - .offset:         872
        .size:           8
        .value_kind:     hidden_global_offset_y
      - .offset:         880
        .size:           8
        .value_kind:     hidden_global_offset_z
      - .offset:         888
        .size:           2
        .value_kind:     hidden_grid_dims
      - .offset:         944
        .size:           4
        .value_kind:     hidden_dynamic_lds_size
    .group_segment_fixed_size: 0
    .kernarg_segment_align: 8
    .kernarg_segment_size: 1080
    .language:       OpenCL C
    .language_version:
      - 2
      - 0
    .max_flat_workgroup_size: 512
    .name:           _Z10hybrid_fwd6Params
    .private_segment_fixed_size: 0
    .sgpr_count:     104
    .sgpr_spill_count: 200
    .symbol:         _Z10hybrid_fwd6Params.kd
    .uniform_work_group_size: 1
    .uses_dynamic_stack: false
    .vgpr_count:     256
    .vgpr_spill_count: 0
    .wavefront_size: 64
